# baseline + 64-byte alignment of the seven GEMM K-loop heads only
# baseline (speedup 1.0000x reference)
.LBB0_286:
	s_lshl_b32 s10, s51, 19
	s_add_u32 s10, s20, s10
	s_addc_u32 s11, s21, 0
	s_and_b64 s[16:17], s[4:5], exec
	s_cselect_b32 s54, s11, s31
	s_cselect_b32 s55, s10, s30
	s_lshl_b32 s14, s50, 19
	s_add_u32 s16, s15, s14
	s_addc_u32 s17, s26, 0
	s_and_b64 s[36:37], s[4:5], exec
	s_cselect_b32 s56, s17, s23
	s_cselect_b32 s57, s16, s22
	s_add_i32 s60, 0, 0x10000
	v_add_u32_e32 v198, s60, v196
	s_add_i32 s62, 0, 0x14000
	v_add_u32_e32 v199, s62, v196
	ds_read_b128 v[160:163], v198
	ds_read_b128 v[152:155], v198 offset:1024
	ds_read_b128 v[156:159], v198 offset:2048
	ds_read_b128 v[148:151], v198 offset:3072
	ds_read_b128 v[144:147], v199
	ds_read_b128 v[136:139], v199 offset:1024
	ds_read_b128 v[140:143], v199 offset:2048
	ds_read_b128 v[132:135], v199 offset:3072
	s_add_u32 s36, s30, 0x40080
	s_addc_u32 s37, s31, 0
	s_add_i32 s58, s41, 0xc000
	v_lshl_add_u64 v[174:175], s[36:37], 0, v[168:169]
	s_mov_b32 m0, s58
	s_add_i32 s59, s41, 0xe000
	ds_read_b128 v[178:181], v197
	ds_read_b128 v[182:185], v197 offset:1024
	ds_read_b128 v[190:193], v197 offset:2048
	ds_read_b128 v[200:203], v197 offset:3072
	ds_read_b128 v[204:207], v197 offset:4096
	ds_read_b128 v[208:211], v197 offset:5120
	ds_read_b128 v[212:215], v197 offset:6144
	ds_read_b128 v[216:219], v197 offset:7168
	global_load_lds_dwordx4 v[174:175], off
	v_lshl_add_u64 v[174:175], s[36:37], 0, v[166:167]
	s_mov_b32 m0, s59
	s_nop 0
	global_load_lds_dwordx4 v[174:175], off
	s_waitcnt vmcnt(8)
	s_waitcnt lgkmcnt(0)
	s_barrier
	s_setprio 1
	s_waitcnt lgkmcnt(0)
	v_mfma_f32_16x16x32_bf16 v[128:131], v[160:163], v[178:181], 0
	v_mfma_f32_16x16x32_bf16 v[124:127], v[156:159], v[178:181], 0
	v_mfma_f32_16x16x32_bf16 v[120:123], v[160:163], v[190:193], 0
	v_mfma_f32_16x16x32_bf16 v[116:119], v[156:159], v[190:193], 0
	v_mfma_f32_16x16x32_bf16 v[112:115], v[160:163], v[204:207], 0
	v_mfma_f32_16x16x32_bf16 v[108:111], v[156:159], v[204:207], 0
	v_mfma_f32_16x16x32_bf16 v[104:107], v[160:163], v[212:215], 0
	v_mfma_f32_16x16x32_bf16 v[100:103], v[156:159], v[212:215], 0
	s_nop 0
	v_mfma_f32_16x16x32_bf16 v[128:131], v[152:155], v[182:185], v[128:131]
	v_mfma_f32_16x16x32_bf16 v[124:127], v[148:151], v[182:185], v[124:127]
	v_mfma_f32_16x16x32_bf16 v[120:123], v[152:155], v[200:203], v[120:123]
	v_mfma_f32_16x16x32_bf16 v[116:119], v[148:151], v[200:203], v[116:119]
	v_mfma_f32_16x16x32_bf16 v[112:115], v[152:155], v[208:211], v[112:115]
	v_mfma_f32_16x16x32_bf16 v[108:111], v[148:151], v[208:211], v[108:111]
	v_mfma_f32_16x16x32_bf16 v[104:107], v[152:155], v[216:219], v[104:107]
	v_mfma_f32_16x16x32_bf16 v[100:103], v[148:151], v[216:219], v[100:103]
	s_setprio 0
	s_setprio 1
	v_mfma_f32_16x16x32_bf16 v[96:99], v[144:147], v[178:181], 0
	v_mfma_f32_16x16x32_bf16 v[92:95], v[140:143], v[178:181], 0
	v_mfma_f32_16x16x32_bf16 v[88:91], v[144:147], v[190:193], 0
	v_mfma_f32_16x16x32_bf16 v[84:87], v[140:143], v[190:193], 0
	v_mfma_f32_16x16x32_bf16 v[80:83], v[144:147], v[204:207], 0
	v_mfma_f32_16x16x32_bf16 v[76:79], v[140:143], v[204:207], 0
	v_mfma_f32_16x16x32_bf16 v[72:75], v[144:147], v[212:215], 0
	v_mfma_f32_16x16x32_bf16 v[68:71], v[140:143], v[212:215], 0
	s_nop 0
	v_mfma_f32_16x16x32_bf16 v[96:99], v[136:139], v[182:185], v[96:99]
	v_mfma_f32_16x16x32_bf16 v[92:95], v[132:135], v[182:185], v[92:95]
	v_mfma_f32_16x16x32_bf16 v[88:91], v[136:139], v[200:203], v[88:91]
	v_mfma_f32_16x16x32_bf16 v[84:87], v[132:135], v[200:203], v[84:87]
	v_mfma_f32_16x16x32_bf16 v[80:83], v[136:139], v[208:211], v[80:83]
	v_mfma_f32_16x16x32_bf16 v[76:79], v[132:135], v[208:211], v[76:79]
	v_mfma_f32_16x16x32_bf16 v[72:75], v[136:139], v[216:219], v[72:75]
	v_mfma_f32_16x16x32_bf16 v[68:71], v[132:135], v[216:219], v[68:71]
	s_setprio 0
	s_barrier
	v_lshl_add_u64 v[174:175], s[22:23], 0, v[34:35]
	s_add_i32 s60, s60, s40
	v_lshl_add_u64 v[190:191], v[174:175], 0, s[28:29]
	s_mov_b32 m0, s60
	s_add_i32 s61, s60, 0x2000
	ds_read_b128 v[178:181], v197 offset:16384
	ds_read_b128 v[182:185], v197 offset:17408
	ds_read_b128 v[200:203], v197 offset:18432
	ds_read_b128 v[204:207], v197 offset:19456
	ds_read_b128 v[208:211], v197 offset:20480
	ds_read_b128 v[212:215], v197 offset:21504
	ds_read_b128 v[216:219], v197 offset:22528
	ds_read_b128 v[222:225], v197 offset:23552
	global_load_lds_dwordx4 v[190:191], off
	v_lshl_add_u64 v[190:191], s[22:23], 0, v[164:165]
	s_add_u32 s36, s22, 0x40100
	v_lshl_add_u64 v[192:193], v[190:191], 0, s[28:29]
	s_mov_b32 m0, s61
	s_addc_u32 s37, s23, 0
	s_add_i32 s62, s62, s40
	global_load_lds_dwordx4 v[192:193], off
	v_lshl_add_u64 v[192:193], s[36:37], 0, v[34:35]
	s_mov_b32 m0, s62
	s_add_i32 s63, s62, 0x2000
	global_load_lds_dwordx4 v[192:193], off
	v_lshl_add_u64 v[192:193], s[36:37], 0, v[164:165]
	s_mov_b32 m0, s63
	s_nop 0
	global_load_lds_dwordx4 v[192:193], off
	v_lshl_add_u64 v[192:193], s[30:31], 0, v[168:169]
	v_lshl_add_u64 v[194:195], v[192:193], 0, s[28:29]
	s_mov_b32 m0, s41
	s_nop 0
	global_load_lds_dwordx4 v[194:195], off
	v_lshl_add_u64 v[194:195], s[30:31], 0, v[166:167]
	v_lshl_add_u64 v[226:227], v[194:195], 0, s[28:29]
	s_mov_b32 m0, s42
	s_nop 0
	global_load_lds_dwordx4 v[226:227], off
	s_waitcnt vmcnt(8)
	s_waitcnt lgkmcnt(0)
	s_barrier
	s_setprio 1
	s_waitcnt lgkmcnt(0)
	v_mfma_f32_16x16x32_bf16 v[64:67], v[160:163], v[178:181], 0
	v_mfma_f32_16x16x32_bf16 v[60:63], v[156:159], v[178:181], 0
	v_mfma_f32_16x16x32_bf16 v[56:59], v[160:163], v[200:203], 0
	v_mfma_f32_16x16x32_bf16 v[52:55], v[156:159], v[200:203], 0
	v_mfma_f32_16x16x32_bf16 v[48:51], v[160:163], v[208:211], 0
	v_mfma_f32_16x16x32_bf16 v[44:47], v[156:159], v[208:211], 0
	v_mfma_f32_16x16x32_bf16 v[40:43], v[160:163], v[216:219], 0
	v_mfma_f32_16x16x32_bf16 v[36:39], v[156:159], v[216:219], 0
	s_nop 0
	v_mfma_f32_16x16x32_bf16 v[64:67], v[152:155], v[182:185], v[64:67]
	v_mfma_f32_16x16x32_bf16 v[60:63], v[148:151], v[182:185], v[60:63]
	v_mfma_f32_16x16x32_bf16 v[56:59], v[152:155], v[204:207], v[56:59]
	v_mfma_f32_16x16x32_bf16 v[52:55], v[148:151], v[204:207], v[52:55]
	v_mfma_f32_16x16x32_bf16 v[48:51], v[152:155], v[212:215], v[48:51]
	v_mfma_f32_16x16x32_bf16 v[44:47], v[148:151], v[212:215], v[44:47]
	v_mfma_f32_16x16x32_bf16 v[40:43], v[152:155], v[222:225], v[40:43]
	v_mfma_f32_16x16x32_bf16 v[36:39], v[148:151], v[222:225], v[36:39]
	s_setprio 0
	s_setprio 1
	v_mfma_f32_16x16x32_bf16 v[30:33], v[144:147], v[178:181], 0
	v_mfma_f32_16x16x32_bf16 v[26:29], v[140:143], v[178:181], 0
	v_mfma_f32_16x16x32_bf16 v[22:25], v[144:147], v[200:203], 0
	v_mfma_f32_16x16x32_bf16 v[18:21], v[140:143], v[200:203], 0
	v_mfma_f32_16x16x32_bf16 v[14:17], v[144:147], v[208:211], 0
	v_mfma_f32_16x16x32_bf16 v[10:13], v[140:143], v[208:211], 0
	v_mfma_f32_16x16x32_bf16 v[6:9], v[144:147], v[216:219], 0
	v_mfma_f32_16x16x32_bf16 v[2:5], v[140:143], v[216:219], 0
	s_nop 0
	v_mfma_f32_16x16x32_bf16 v[30:33], v[136:139], v[182:185], v[30:33]
	v_mfma_f32_16x16x32_bf16 v[26:29], v[132:135], v[182:185], v[26:29]
	v_mfma_f32_16x16x32_bf16 v[22:25], v[136:139], v[204:207], v[22:25]
	v_mfma_f32_16x16x32_bf16 v[18:21], v[132:135], v[204:207], v[18:21]
	v_mfma_f32_16x16x32_bf16 v[14:17], v[136:139], v[212:215], v[14:17]
	v_mfma_f32_16x16x32_bf16 v[10:13], v[132:135], v[212:215], v[10:13]
	v_mfma_f32_16x16x32_bf16 v[6:9], v[136:139], v[222:225], v[6:9]
	v_mfma_f32_16x16x32_bf16 v[2:5], v[132:135], v[222:225], v[2:5]
	s_setprio 0
	s_barrier
	s_add_i32 s64, 0, 0x18000
	s_add_i32 s66, 0, 0x1c000
	v_add_u32_e32 v132, s64, v196
	v_add_u32_e32 v133, s66, v196
	ds_read_b128 v[134:137], v132
	ds_read_b128 v[138:141], v132 offset:1024
	ds_read_b128 v[142:145], v132 offset:2048
	ds_read_b128 v[146:149], v132 offset:3072
	ds_read_b128 v[150:153], v133
	ds_read_b128 v[154:157], v133 offset:1024
	ds_read_b128 v[158:161], v133 offset:2048
	ds_read_b128 v[178:181], v133 offset:3072
	s_add_u32 s36, s30, 0x40100
	s_addc_u32 s37, s31, 0
	s_mov_b32 m0, s43
	v_lshl_add_u64 v[162:163], s[36:37], 0, v[168:169]
	ds_read_b128 v[182:185], v197 offset:32768
	ds_read_b128 v[200:203], v197 offset:33792
	ds_read_b128 v[204:207], v197 offset:34816
	ds_read_b128 v[208:211], v197 offset:35840
	ds_read_b128 v[212:215], v197 offset:36864
	ds_read_b128 v[216:219], v197 offset:37888
	ds_read_b128 v[222:225], v197 offset:38912
	ds_read_b128 v[226:229], v197 offset:39936
	global_load_lds_dwordx4 v[162:163], off
	v_lshl_add_u64 v[162:163], s[36:37], 0, v[166:167]
	s_mov_b32 m0, s44
	s_nop 0
	global_load_lds_dwordx4 v[162:163], off
	s_waitcnt vmcnt(8)
	s_waitcnt lgkmcnt(0)
	s_barrier
	s_setprio 1
	s_waitcnt lgkmcnt(0)
	v_mfma_f32_16x16x32_bf16 v[128:131], v[134:137], v[182:185], v[128:131]
	v_mfma_f32_16x16x32_bf16 v[124:127], v[142:145], v[182:185], v[124:127]
	v_mfma_f32_16x16x32_bf16 v[120:123], v[134:137], v[204:207], v[120:123]
	v_mfma_f32_16x16x32_bf16 v[116:119], v[142:145], v[204:207], v[116:119]
	v_mfma_f32_16x16x32_bf16 v[112:115], v[134:137], v[212:215], v[112:115]
	v_mfma_f32_16x16x32_bf16 v[108:111], v[142:145], v[212:215], v[108:111]
	v_mfma_f32_16x16x32_bf16 v[104:107], v[134:137], v[222:225], v[104:107]
	v_mfma_f32_16x16x32_bf16 v[100:103], v[142:145], v[222:225], v[100:103]
	v_mfma_f32_16x16x32_bf16 v[128:131], v[138:141], v[200:203], v[128:131]
	v_mfma_f32_16x16x32_bf16 v[124:127], v[146:149], v[200:203], v[124:127]
	v_mfma_f32_16x16x32_bf16 v[120:123], v[138:141], v[208:211], v[120:123]
	v_mfma_f32_16x16x32_bf16 v[116:119], v[146:149], v[208:211], v[116:119]
	v_mfma_f32_16x16x32_bf16 v[112:115], v[138:141], v[216:219], v[112:115]
	v_mfma_f32_16x16x32_bf16 v[108:111], v[146:149], v[216:219], v[108:111]
	v_mfma_f32_16x16x32_bf16 v[104:107], v[138:141], v[226:229], v[104:107]
	v_mfma_f32_16x16x32_bf16 v[100:103], v[146:149], v[226:229], v[100:103]
	s_setprio 0
	s_setprio 1
	v_mfma_f32_16x16x32_bf16 v[96:99], v[150:153], v[182:185], v[96:99]
	v_mfma_f32_16x16x32_bf16 v[92:95], v[158:161], v[182:185], v[92:95]
	v_mfma_f32_16x16x32_bf16 v[88:91], v[150:153], v[204:207], v[88:91]
	v_mfma_f32_16x16x32_bf16 v[84:87], v[158:161], v[204:207], v[84:87]
	v_mfma_f32_16x16x32_bf16 v[80:83], v[150:153], v[212:215], v[80:83]
	v_mfma_f32_16x16x32_bf16 v[76:79], v[158:161], v[212:215], v[76:79]
	v_mfma_f32_16x16x32_bf16 v[72:75], v[150:153], v[222:225], v[72:75]
	v_mfma_f32_16x16x32_bf16 v[68:71], v[158:161], v[222:225], v[68:71]
	v_mfma_f32_16x16x32_bf16 v[96:99], v[154:157], v[200:203], v[96:99]
	v_mfma_f32_16x16x32_bf16 v[92:95], v[178:181], v[200:203], v[92:95]
	v_mfma_f32_16x16x32_bf16 v[88:91], v[154:157], v[208:211], v[88:91]
	v_mfma_f32_16x16x32_bf16 v[84:87], v[178:181], v[208:211], v[84:87]
	v_mfma_f32_16x16x32_bf16 v[80:83], v[154:157], v[216:219], v[80:83]
	v_mfma_f32_16x16x32_bf16 v[76:79], v[178:181], v[216:219], v[76:79]
	v_mfma_f32_16x16x32_bf16 v[72:75], v[154:157], v[226:229], v[72:75]
	v_mfma_f32_16x16x32_bf16 v[68:71], v[178:181], v[226:229], v[68:71]
	s_setprio 0
	s_barrier
	s_add_i32 s64, s64, s40
	s_mov_b64 s[24:25], 0x180
	s_add_i32 s65, s64, 0x2000
	v_lshl_add_u64 v[162:163], v[174:175], 0, s[24:25]
	s_mov_b32 m0, s64
	s_add_u32 s36, s22, 0x40180
	ds_read_b128 v[182:185], v197 offset:49152
	ds_read_b128 v[200:203], v197 offset:50176
	ds_read_b128 v[204:207], v197 offset:51200
	ds_read_b128 v[208:211], v197 offset:52224
	ds_read_b128 v[212:215], v197 offset:53248
	ds_read_b128 v[216:219], v197 offset:54272
	ds_read_b128 v[222:225], v197 offset:55296
	ds_read_b128 v[226:229], v197 offset:56320
	global_load_lds_dwordx4 v[162:163], off
	v_lshl_add_u64 v[162:163], v[190:191], 0, s[24:25]
	s_mov_b32 m0, s65
	s_addc_u32 s37, s23, 0
	s_add_i32 s66, s66, s40
	global_load_lds_dwordx4 v[162:163], off
	v_lshl_add_u64 v[162:163], s[36:37], 0, v[34:35]
	s_mov_b32 m0, s66
	s_add_i32 s67, s66, 0x2000
	global_load_lds_dwordx4 v[162:163], off
	v_lshl_add_u64 v[162:163], s[36:37], 0, v[164:165]
	s_mov_b32 m0, s67
	s_nop 0
	global_load_lds_dwordx4 v[162:163], off
	v_lshl_add_u64 v[162:163], v[192:193], 0, s[24:25]
	s_mov_b32 m0, s47
	s_nop 0
	global_load_lds_dwordx4 v[162:163], off
	v_lshl_add_u64 v[162:163], v[194:195], 0, s[24:25]
	s_mov_b32 m0, s48
	s_nop 0
	global_load_lds_dwordx4 v[162:163], off
	s_waitcnt vmcnt(8)
	s_waitcnt lgkmcnt(0)
	s_barrier
	s_setprio 1
	s_waitcnt lgkmcnt(0)
	v_mfma_f32_16x16x32_bf16 v[64:67], v[134:137], v[182:185], v[64:67]
	v_mfma_f32_16x16x32_bf16 v[60:63], v[142:145], v[182:185], v[60:63]
	v_mfma_f32_16x16x32_bf16 v[56:59], v[134:137], v[204:207], v[56:59]
	v_mfma_f32_16x16x32_bf16 v[52:55], v[142:145], v[204:207], v[52:55]
	v_mfma_f32_16x16x32_bf16 v[48:51], v[134:137], v[212:215], v[48:51]
	v_mfma_f32_16x16x32_bf16 v[44:47], v[142:145], v[212:215], v[44:47]
	v_mfma_f32_16x16x32_bf16 v[40:43], v[134:137], v[222:225], v[40:43]
	v_mfma_f32_16x16x32_bf16 v[36:39], v[142:145], v[222:225], v[36:39]
	v_mfma_f32_16x16x32_bf16 v[64:67], v[138:141], v[200:203], v[64:67]
	v_mfma_f32_16x16x32_bf16 v[60:63], v[146:149], v[200:203], v[60:63]
	v_mfma_f32_16x16x32_bf16 v[56:59], v[138:141], v[208:211], v[56:59]
	v_mfma_f32_16x16x32_bf16 v[52:55], v[146:149], v[208:211], v[52:55]
	v_mfma_f32_16x16x32_bf16 v[48:51], v[138:141], v[216:219], v[48:51]
	v_mfma_f32_16x16x32_bf16 v[44:47], v[146:149], v[216:219], v[44:47]
	v_mfma_f32_16x16x32_bf16 v[40:43], v[138:141], v[226:229], v[40:43]
	v_mfma_f32_16x16x32_bf16 v[36:39], v[146:149], v[226:229], v[36:39]
	s_setprio 0
	s_setprio 1
	v_mfma_f32_16x16x32_bf16 v[30:33], v[150:153], v[182:185], v[30:33]
	v_mfma_f32_16x16x32_bf16 v[26:29], v[158:161], v[182:185], v[26:29]
	v_mfma_f32_16x16x32_bf16 v[22:25], v[150:153], v[204:207], v[22:25]
	v_mfma_f32_16x16x32_bf16 v[18:21], v[158:161], v[204:207], v[18:21]
	v_mfma_f32_16x16x32_bf16 v[14:17], v[150:153], v[212:215], v[14:17]
	v_mfma_f32_16x16x32_bf16 v[10:13], v[158:161], v[212:215], v[10:13]
	v_mfma_f32_16x16x32_bf16 v[6:9], v[150:153], v[222:225], v[6:9]
	v_mfma_f32_16x16x32_bf16 v[2:5], v[158:161], v[222:225], v[2:5]
	v_mfma_f32_16x16x32_bf16 v[30:33], v[154:157], v[200:203], v[30:33]
	v_mfma_f32_16x16x32_bf16 v[26:29], v[178:181], v[200:203], v[26:29]
	v_mfma_f32_16x16x32_bf16 v[22:25], v[154:157], v[208:211], v[22:25]
	v_mfma_f32_16x16x32_bf16 v[18:21], v[178:181], v[208:211], v[18:21]
	v_mfma_f32_16x16x32_bf16 v[14:17], v[154:157], v[216:219], v[14:17]
	v_mfma_f32_16x16x32_bf16 v[10:13], v[178:181], v[216:219], v[10:13]
	v_mfma_f32_16x16x32_bf16 v[6:9], v[154:157], v[226:229], v[6:9]
	v_mfma_f32_16x16x32_bf16 v[2:5], v[178:181], v[226:229], v[2:5]
	s_setprio 0
	s_barrier
	s_add_u32 s30, s30, 0x40180
	s_addc_u32 s31, s31, 0
	s_add_u32 s68, s22, 0x200
	s_addc_u32 s69, s23, 0
	s_mov_b32 s70, 0
	.p2align	6

.LBB0_540:
	s_lshl_b32 s14, s55, 19
	v_readlane_b32 s16, v253, 53
	v_readlane_b32 s17, v253, 54
	s_add_u32 s16, s16, s14
	s_addc_u32 s17, s17, 0
	s_and_b64 s[22:23], s[4:5], exec
	s_cselect_b32 s58, s17, s37
	s_cselect_b32 s59, s16, s36
	s_lshl_b32 s14, s54, 19
	s_add_u32 s22, s15, s14
	s_addc_u32 s23, s26, 0
	s_and_b64 s[40:41], s[4:5], exec
	s_cselect_b32 s60, s23, s31
	s_cselect_b32 s61, s22, s30
	s_add_i32 s64, 0, 0x10000
	v_add_u32_e32 v172, s64, v222
	s_add_i32 s66, 0, 0x14000
	v_add_u32_e32 v173, s66, v222
	ds_read_b128 v[160:163], v172
	ds_read_b128 v[152:155], v172 offset:1024
	ds_read_b128 v[156:159], v172 offset:2048
	ds_read_b128 v[148:151], v172 offset:3072
	ds_read_b128 v[144:147], v173
	ds_read_b128 v[136:139], v173 offset:1024
	ds_read_b128 v[140:143], v173 offset:2048
	ds_read_b128 v[132:135], v173 offset:3072
	s_add_u32 s40, s36, 0x40080
	s_addc_u32 s41, s37, 0
	s_add_i32 s62, s43, 0xc000
	v_lshl_add_u64 v[174:175], s[40:41], 0, v[194:195]
	s_mov_b32 m0, s62
	s_add_i32 s63, s43, 0xe000
	ds_read_b128 v[164:167], v223
	ds_read_b128 v[168:171], v223 offset:1024
	ds_read_b128 v[178:181], v223 offset:2048
	ds_read_b128 v[182:185], v223 offset:3072
	ds_read_b128 v[200:203], v223 offset:4096
	ds_read_b128 v[204:207], v223 offset:5120
	ds_read_b128 v[208:211], v223 offset:6144
	ds_read_b128 v[212:215], v223 offset:7168
	global_load_lds_dwordx4 v[174:175], off
	v_lshl_add_u64 v[174:175], s[40:41], 0, v[192:193]
	s_mov_b32 m0, s63
	s_nop 0
	global_load_lds_dwordx4 v[174:175], off
	s_waitcnt vmcnt(8)
	s_waitcnt lgkmcnt(0)
	s_barrier
	s_setprio 1
	s_waitcnt lgkmcnt(0)
	v_mfma_f32_16x16x32_bf16 v[128:131], v[160:163], v[164:167], 0
	v_mfma_f32_16x16x32_bf16 v[124:127], v[156:159], v[164:167], 0
	v_mfma_f32_16x16x32_bf16 v[120:123], v[160:163], v[178:181], 0
	v_mfma_f32_16x16x32_bf16 v[116:119], v[156:159], v[178:181], 0
	v_mfma_f32_16x16x32_bf16 v[112:115], v[160:163], v[200:203], 0
	v_mfma_f32_16x16x32_bf16 v[108:111], v[156:159], v[200:203], 0
	v_mfma_f32_16x16x32_bf16 v[104:107], v[160:163], v[208:211], 0
	v_mfma_f32_16x16x32_bf16 v[100:103], v[156:159], v[208:211], 0
	s_nop 0
	v_mfma_f32_16x16x32_bf16 v[128:131], v[152:155], v[168:171], v[128:131]
	v_mfma_f32_16x16x32_bf16 v[124:127], v[148:151], v[168:171], v[124:127]
	v_mfma_f32_16x16x32_bf16 v[120:123], v[152:155], v[182:185], v[120:123]
	v_mfma_f32_16x16x32_bf16 v[116:119], v[148:151], v[182:185], v[116:119]
	v_mfma_f32_16x16x32_bf16 v[112:115], v[152:155], v[204:207], v[112:115]
	v_mfma_f32_16x16x32_bf16 v[108:111], v[148:151], v[204:207], v[108:111]
	v_mfma_f32_16x16x32_bf16 v[104:107], v[152:155], v[212:215], v[104:107]
	v_mfma_f32_16x16x32_bf16 v[100:103], v[148:151], v[212:215], v[100:103]
	s_setprio 0
	s_setprio 1
	v_mfma_f32_16x16x32_bf16 v[96:99], v[144:147], v[164:167], 0
	v_mfma_f32_16x16x32_bf16 v[92:95], v[140:143], v[164:167], 0
	v_mfma_f32_16x16x32_bf16 v[88:91], v[144:147], v[178:181], 0
	v_mfma_f32_16x16x32_bf16 v[84:87], v[140:143], v[178:181], 0
	v_mfma_f32_16x16x32_bf16 v[80:83], v[144:147], v[200:203], 0
	v_mfma_f32_16x16x32_bf16 v[76:79], v[140:143], v[200:203], 0
	v_mfma_f32_16x16x32_bf16 v[72:75], v[144:147], v[208:211], 0
	v_mfma_f32_16x16x32_bf16 v[68:71], v[140:143], v[208:211], 0
	s_nop 0
	v_mfma_f32_16x16x32_bf16 v[96:99], v[136:139], v[168:171], v[96:99]
	v_mfma_f32_16x16x32_bf16 v[92:95], v[132:135], v[168:171], v[92:95]
	v_mfma_f32_16x16x32_bf16 v[88:91], v[136:139], v[182:185], v[88:91]
	v_mfma_f32_16x16x32_bf16 v[84:87], v[132:135], v[182:185], v[84:87]
	v_mfma_f32_16x16x32_bf16 v[80:83], v[136:139], v[204:207], v[80:83]
	v_mfma_f32_16x16x32_bf16 v[76:79], v[132:135], v[204:207], v[76:79]
	v_mfma_f32_16x16x32_bf16 v[72:75], v[136:139], v[212:215], v[72:75]
	v_mfma_f32_16x16x32_bf16 v[68:71], v[132:135], v[212:215], v[68:71]
	s_setprio 0
	s_barrier
	v_lshl_add_u64 v[164:165], s[30:31], 0, v[34:35]
	s_add_i32 s64, s64, s42
	v_lshl_add_u64 v[166:167], v[164:165], 0, s[28:29]
	s_mov_b32 m0, s64
	s_add_i32 s65, s64, 0x2000
	ds_read_b128 v[178:181], v223 offset:16384
	ds_read_b128 v[182:185], v223 offset:17408
	ds_read_b128 v[200:203], v223 offset:18432
	ds_read_b128 v[204:207], v223 offset:19456
	ds_read_b128 v[208:211], v223 offset:20480
	ds_read_b128 v[212:215], v223 offset:21504
	ds_read_b128 v[216:219], v223 offset:22528
	ds_read_b128 v[224:227], v223 offset:23552
	global_load_lds_dwordx4 v[166:167], off
	v_lshl_add_u64 v[166:167], s[30:31], 0, v[190:191]
	s_add_u32 s40, s30, 0x40100
	v_lshl_add_u64 v[168:169], v[166:167], 0, s[28:29]
	s_mov_b32 m0, s65
	s_addc_u32 s41, s31, 0
	s_add_i32 s66, s66, s42
	global_load_lds_dwordx4 v[168:169], off
	v_lshl_add_u64 v[168:169], s[40:41], 0, v[34:35]
	s_mov_b32 m0, s66
	s_add_i32 s67, s66, 0x2000
	global_load_lds_dwordx4 v[168:169], off
	v_lshl_add_u64 v[168:169], s[40:41], 0, v[190:191]
	s_mov_b32 m0, s67
	s_nop 0
	global_load_lds_dwordx4 v[168:169], off
	v_lshl_add_u64 v[168:169], s[36:37], 0, v[194:195]
	v_lshl_add_u64 v[170:171], v[168:169], 0, s[28:29]
	s_mov_b32 m0, s43
	s_nop 0
	global_load_lds_dwordx4 v[170:171], off
	v_lshl_add_u64 v[170:171], s[36:37], 0, v[192:193]
	v_lshl_add_u64 v[174:175], v[170:171], 0, s[28:29]
	s_mov_b32 m0, s44
	s_nop 0
	global_load_lds_dwordx4 v[174:175], off
	s_waitcnt vmcnt(8)
	s_waitcnt lgkmcnt(0)
	s_barrier
	s_setprio 1
	s_waitcnt lgkmcnt(0)
	v_mfma_f32_16x16x32_bf16 v[64:67], v[160:163], v[178:181], 0
	v_mfma_f32_16x16x32_bf16 v[60:63], v[156:159], v[178:181], 0
	v_mfma_f32_16x16x32_bf16 v[56:59], v[160:163], v[200:203], 0
	v_mfma_f32_16x16x32_bf16 v[52:55], v[156:159], v[200:203], 0
	v_mfma_f32_16x16x32_bf16 v[48:51], v[160:163], v[208:211], 0
	v_mfma_f32_16x16x32_bf16 v[44:47], v[156:159], v[208:211], 0
	v_mfma_f32_16x16x32_bf16 v[40:43], v[160:163], v[216:219], 0
	v_mfma_f32_16x16x32_bf16 v[36:39], v[156:159], v[216:219], 0
	s_nop 0
	v_mfma_f32_16x16x32_bf16 v[64:67], v[152:155], v[182:185], v[64:67]
	v_mfma_f32_16x16x32_bf16 v[60:63], v[148:151], v[182:185], v[60:63]
	v_mfma_f32_16x16x32_bf16 v[56:59], v[152:155], v[204:207], v[56:59]
	v_mfma_f32_16x16x32_bf16 v[52:55], v[148:151], v[204:207], v[52:55]
	v_mfma_f32_16x16x32_bf16 v[48:51], v[152:155], v[212:215], v[48:51]
	v_mfma_f32_16x16x32_bf16 v[44:47], v[148:151], v[212:215], v[44:47]
	v_mfma_f32_16x16x32_bf16 v[40:43], v[152:155], v[224:227], v[40:43]
	v_mfma_f32_16x16x32_bf16 v[36:39], v[148:151], v[224:227], v[36:39]
	s_setprio 0
	s_setprio 1
	v_mfma_f32_16x16x32_bf16 v[30:33], v[144:147], v[178:181], 0
	v_mfma_f32_16x16x32_bf16 v[26:29], v[140:143], v[178:181], 0
	v_mfma_f32_16x16x32_bf16 v[22:25], v[144:147], v[200:203], 0
	v_mfma_f32_16x16x32_bf16 v[18:21], v[140:143], v[200:203], 0
	v_mfma_f32_16x16x32_bf16 v[14:17], v[144:147], v[208:211], 0
	v_mfma_f32_16x16x32_bf16 v[10:13], v[140:143], v[208:211], 0
	v_mfma_f32_16x16x32_bf16 v[6:9], v[144:147], v[216:219], 0
	v_mfma_f32_16x16x32_bf16 v[2:5], v[140:143], v[216:219], 0
	s_nop 0
	v_mfma_f32_16x16x32_bf16 v[30:33], v[136:139], v[182:185], v[30:33]
	v_mfma_f32_16x16x32_bf16 v[26:29], v[132:135], v[182:185], v[26:29]
	v_mfma_f32_16x16x32_bf16 v[22:25], v[136:139], v[204:207], v[22:25]
	v_mfma_f32_16x16x32_bf16 v[18:21], v[132:135], v[204:207], v[18:21]
	v_mfma_f32_16x16x32_bf16 v[14:17], v[136:139], v[212:215], v[14:17]
	v_mfma_f32_16x16x32_bf16 v[10:13], v[132:135], v[212:215], v[10:13]
	v_mfma_f32_16x16x32_bf16 v[6:9], v[136:139], v[224:227], v[6:9]
	v_mfma_f32_16x16x32_bf16 v[2:5], v[132:135], v[224:227], v[2:5]
	s_setprio 0
	s_barrier
	s_add_i32 s68, 0, 0x18000
	s_add_i32 s70, 0, 0x1c000
	v_add_u32_e32 v132, s68, v222
	v_add_u32_e32 v133, s70, v222
	ds_read_b128 v[134:137], v132
	ds_read_b128 v[138:141], v132 offset:1024
	ds_read_b128 v[142:145], v132 offset:2048
	ds_read_b128 v[146:149], v132 offset:3072
	ds_read_b128 v[150:153], v133
	ds_read_b128 v[154:157], v133 offset:1024
	ds_read_b128 v[158:161], v133 offset:2048
	ds_read_b128 v[178:181], v133 offset:3072
	s_add_u32 s40, s36, 0x40100
	s_addc_u32 s41, s37, 0
	s_mov_b32 m0, s45
	v_lshl_add_u64 v[162:163], s[40:41], 0, v[194:195]
	ds_read_b128 v[182:185], v223 offset:32768
	ds_read_b128 v[200:203], v223 offset:33792
	ds_read_b128 v[204:207], v223 offset:34816
	ds_read_b128 v[208:211], v223 offset:35840
	ds_read_b128 v[212:215], v223 offset:36864
	ds_read_b128 v[216:219], v223 offset:37888
	ds_read_b128 v[224:227], v223 offset:38912
	ds_read_b128 v[228:231], v223 offset:39936
	global_load_lds_dwordx4 v[162:163], off
	v_lshl_add_u64 v[162:163], s[40:41], 0, v[192:193]
	s_mov_b32 m0, s46
	s_nop 0
	global_load_lds_dwordx4 v[162:163], off
	s_waitcnt vmcnt(8)
	s_waitcnt lgkmcnt(0)
	s_barrier
	s_setprio 1
	s_waitcnt lgkmcnt(0)
	v_mfma_f32_16x16x32_bf16 v[128:131], v[134:137], v[182:185], v[128:131]
	v_mfma_f32_16x16x32_bf16 v[124:127], v[142:145], v[182:185], v[124:127]
	v_mfma_f32_16x16x32_bf16 v[120:123], v[134:137], v[204:207], v[120:123]
	v_mfma_f32_16x16x32_bf16 v[116:119], v[142:145], v[204:207], v[116:119]
	v_mfma_f32_16x16x32_bf16 v[112:115], v[134:137], v[212:215], v[112:115]
	v_mfma_f32_16x16x32_bf16 v[108:111], v[142:145], v[212:215], v[108:111]
	v_mfma_f32_16x16x32_bf16 v[104:107], v[134:137], v[224:227], v[104:107]
	v_mfma_f32_16x16x32_bf16 v[100:103], v[142:145], v[224:227], v[100:103]
	v_mfma_f32_16x16x32_bf16 v[128:131], v[138:141], v[200:203], v[128:131]
	v_mfma_f32_16x16x32_bf16 v[124:127], v[146:149], v[200:203], v[124:127]
	v_mfma_f32_16x16x32_bf16 v[120:123], v[138:141], v[208:211], v[120:123]
	v_mfma_f32_16x16x32_bf16 v[116:119], v[146:149], v[208:211], v[116:119]
	v_mfma_f32_16x16x32_bf16 v[112:115], v[138:141], v[216:219], v[112:115]
	v_mfma_f32_16x16x32_bf16 v[108:111], v[146:149], v[216:219], v[108:111]
	v_mfma_f32_16x16x32_bf16 v[104:107], v[138:141], v[228:231], v[104:107]
	v_mfma_f32_16x16x32_bf16 v[100:103], v[146:149], v[228:231], v[100:103]
	s_setprio 0
	s_setprio 1
	v_mfma_f32_16x16x32_bf16 v[96:99], v[150:153], v[182:185], v[96:99]
	v_mfma_f32_16x16x32_bf16 v[92:95], v[158:161], v[182:185], v[92:95]
	v_mfma_f32_16x16x32_bf16 v[88:91], v[150:153], v[204:207], v[88:91]
	v_mfma_f32_16x16x32_bf16 v[84:87], v[158:161], v[204:207], v[84:87]
	v_mfma_f32_16x16x32_bf16 v[80:83], v[150:153], v[212:215], v[80:83]
	v_mfma_f32_16x16x32_bf16 v[76:79], v[158:161], v[212:215], v[76:79]
	v_mfma_f32_16x16x32_bf16 v[72:75], v[150:153], v[224:227], v[72:75]
	v_mfma_f32_16x16x32_bf16 v[68:71], v[158:161], v[224:227], v[68:71]
	v_mfma_f32_16x16x32_bf16 v[96:99], v[154:157], v[200:203], v[96:99]
	v_mfma_f32_16x16x32_bf16 v[92:95], v[178:181], v[200:203], v[92:95]
	v_mfma_f32_16x16x32_bf16 v[88:91], v[154:157], v[208:211], v[88:91]
	v_mfma_f32_16x16x32_bf16 v[84:87], v[178:181], v[208:211], v[84:87]
	v_mfma_f32_16x16x32_bf16 v[80:83], v[154:157], v[216:219], v[80:83]
	v_mfma_f32_16x16x32_bf16 v[76:79], v[178:181], v[216:219], v[76:79]
	v_mfma_f32_16x16x32_bf16 v[72:75], v[154:157], v[228:231], v[72:75]
	v_mfma_f32_16x16x32_bf16 v[68:71], v[178:181], v[228:231], v[68:71]
	s_setprio 0
	s_barrier
	s_add_i32 s68, s68, s42
	s_mov_b64 s[24:25], 0x180
	s_add_i32 s69, s68, 0x2000
	v_lshl_add_u64 v[162:163], v[164:165], 0, s[24:25]
	s_mov_b32 m0, s68
	s_add_u32 s40, s30, 0x40180
	ds_read_b128 v[182:185], v223 offset:49152
	ds_read_b128 v[200:203], v223 offset:50176
	ds_read_b128 v[204:207], v223 offset:51200
	ds_read_b128 v[208:211], v223 offset:52224
	ds_read_b128 v[212:215], v223 offset:53248
	ds_read_b128 v[216:219], v223 offset:54272
	ds_read_b128 v[224:227], v223 offset:55296
	ds_read_b128 v[228:231], v223 offset:56320
	global_load_lds_dwordx4 v[162:163], off
	v_lshl_add_u64 v[162:163], v[166:167], 0, s[24:25]
	s_mov_b32 m0, s69
	s_addc_u32 s41, s31, 0
	s_add_i32 s70, s70, s42
	global_load_lds_dwordx4 v[162:163], off
	v_lshl_add_u64 v[162:163], s[40:41], 0, v[34:35]
	s_mov_b32 m0, s70
	s_add_i32 s71, s70, 0x2000
	global_load_lds_dwordx4 v[162:163], off
	v_lshl_add_u64 v[162:163], s[40:41], 0, v[190:191]
	s_mov_b32 m0, s71
	s_nop 0
	global_load_lds_dwordx4 v[162:163], off
	v_lshl_add_u64 v[162:163], v[168:169], 0, s[24:25]
	s_mov_b32 m0, s51
	s_nop 0
	global_load_lds_dwordx4 v[162:163], off
	v_lshl_add_u64 v[162:163], v[170:171], 0, s[24:25]
	s_mov_b32 m0, s52
	s_nop 0
	global_load_lds_dwordx4 v[162:163], off
	s_waitcnt vmcnt(8)
	s_waitcnt lgkmcnt(0)
	s_barrier
	s_setprio 1
	s_waitcnt lgkmcnt(0)
	v_mfma_f32_16x16x32_bf16 v[64:67], v[134:137], v[182:185], v[64:67]
	v_mfma_f32_16x16x32_bf16 v[60:63], v[142:145], v[182:185], v[60:63]
	v_mfma_f32_16x16x32_bf16 v[56:59], v[134:137], v[204:207], v[56:59]
	v_mfma_f32_16x16x32_bf16 v[52:55], v[142:145], v[204:207], v[52:55]
	v_mfma_f32_16x16x32_bf16 v[48:51], v[134:137], v[212:215], v[48:51]
	v_mfma_f32_16x16x32_bf16 v[44:47], v[142:145], v[212:215], v[44:47]
	v_mfma_f32_16x16x32_bf16 v[40:43], v[134:137], v[224:227], v[40:43]
	v_mfma_f32_16x16x32_bf16 v[36:39], v[142:145], v[224:227], v[36:39]
	v_mfma_f32_16x16x32_bf16 v[64:67], v[138:141], v[200:203], v[64:67]
	v_mfma_f32_16x16x32_bf16 v[60:63], v[146:149], v[200:203], v[60:63]
	v_mfma_f32_16x16x32_bf16 v[56:59], v[138:141], v[208:211], v[56:59]
	v_mfma_f32_16x16x32_bf16 v[52:55], v[146:149], v[208:211], v[52:55]
	v_mfma_f32_16x16x32_bf16 v[48:51], v[138:141], v[216:219], v[48:51]
	v_mfma_f32_16x16x32_bf16 v[44:47], v[146:149], v[216:219], v[44:47]
	v_mfma_f32_16x16x32_bf16 v[40:43], v[138:141], v[228:231], v[40:43]
	v_mfma_f32_16x16x32_bf16 v[36:39], v[146:149], v[228:231], v[36:39]
	s_setprio 0
	s_setprio 1
	v_mfma_f32_16x16x32_bf16 v[30:33], v[150:153], v[182:185], v[30:33]
	v_mfma_f32_16x16x32_bf16 v[26:29], v[158:161], v[182:185], v[26:29]
	v_mfma_f32_16x16x32_bf16 v[22:25], v[150:153], v[204:207], v[22:25]
	v_mfma_f32_16x16x32_bf16 v[18:21], v[158:161], v[204:207], v[18:21]
	v_mfma_f32_16x16x32_bf16 v[14:17], v[150:153], v[212:215], v[14:17]
	v_mfma_f32_16x16x32_bf16 v[10:13], v[158:161], v[212:215], v[10:13]
	v_mfma_f32_16x16x32_bf16 v[6:9], v[150:153], v[224:227], v[6:9]
	v_mfma_f32_16x16x32_bf16 v[2:5], v[158:161], v[224:227], v[2:5]
	v_mfma_f32_16x16x32_bf16 v[30:33], v[154:157], v[200:203], v[30:33]
	v_mfma_f32_16x16x32_bf16 v[26:29], v[178:181], v[200:203], v[26:29]
	v_mfma_f32_16x16x32_bf16 v[22:25], v[154:157], v[208:211], v[22:25]
	v_mfma_f32_16x16x32_bf16 v[18:21], v[178:181], v[208:211], v[18:21]
	v_mfma_f32_16x16x32_bf16 v[14:17], v[154:157], v[216:219], v[14:17]
	v_mfma_f32_16x16x32_bf16 v[10:13], v[178:181], v[216:219], v[10:13]
	v_mfma_f32_16x16x32_bf16 v[6:9], v[154:157], v[228:231], v[6:9]
	v_mfma_f32_16x16x32_bf16 v[2:5], v[178:181], v[228:231], v[2:5]
	s_setprio 0
	s_barrier
	s_add_u32 s36, s36, 0x40180
	s_addc_u32 s37, s37, 0
	s_add_u32 s72, s30, 0x200
	s_addc_u32 s73, s31, 0
	s_mov_b32 s74, 0
	.p2align	6

.LBB0_819:
	s_add_u32 s81, s30, 0x200
	s_addc_u32 s82, s31, 0
	s_add_i32 s55, 0, 0x14000
	s_add_i32 s52, 0, 0x10000
	v_add_u32_e32 v199, s55, v167
	v_add_u32_e32 v200, s52, v167
	ds_read_b128 v[10:13], v199
	ds_read_b128 v[14:17], v199 offset:1024
	ds_read_b128 v[2:5], v199 offset:2048
	ds_read_b128 v[6:9], v199 offset:3072
	ds_read_b128 v[22:25], v200 offset:3072
	ds_read_b128 v[18:21], v200 offset:2048
	ds_read_b128 v[30:33], v200 offset:1024
	ds_read_b128 v[26:29], v200
	s_lshl_b32 s14, s80, 10
	s_add_i32 s83, s14, 0
	s_add_i32 s83, s83, 0x20400
	v_mov_b32_e32 v191, v35
	v_mov_b32_e32 v175, v35
	s_add_i32 s84, s69, 0xc000
	v_readlane_b32 s26, v253, 28
	s_mov_b32 m0, s84
	v_readlane_b32 s27, v253, 29
	s_add_i32 s53, s69, 0xe000
	ds_read_b128 v[202:205], v169
	ds_read_b128 v[206:209], v169 offset:1024
	ds_read_b128 v[222:225], v169 offset:2048
	ds_read_b128 v[226:229], v169 offset:3072
	ds_read_b128 v[230:233], v169 offset:4096
	ds_read_b128 v[234:237], v169 offset:5120
	ds_read_b128 v[238:241], v169 offset:6144
	ds_read_b128 v[242:245], v169 offset:7168
	global_load_lds_dwordx4 v190, s[26:27]
	s_mov_b32 m0, s53
	s_nop 0
	global_load_lds_dwordx4 v174, s[26:27]
	s_waitcnt vmcnt(8)
	s_waitcnt lgkmcnt(0)
	s_barrier
	s_setprio 1
	s_waitcnt lgkmcnt(0)
	v_mfma_f32_16x16x128_f8f6f4 v[160:163], v[26:33], v[202:209], 0
	v_mfma_f32_16x16x128_f8f6f4 v[156:159], v[18:25], v[202:209], 0
	v_mfma_f32_16x16x128_f8f6f4 v[152:155], v[26:33], v[222:229], 0
	v_mfma_f32_16x16x128_f8f6f4 v[148:151], v[18:25], v[222:229], 0
	v_mfma_f32_16x16x128_f8f6f4 v[144:147], v[26:33], v[230:237], 0
	v_mfma_f32_16x16x128_f8f6f4 v[140:143], v[18:25], v[230:237], 0
	v_mfma_f32_16x16x128_f8f6f4 v[136:139], v[26:33], v[238:245], 0
	v_mfma_f32_16x16x128_f8f6f4 v[132:135], v[18:25], v[238:245], 0
	s_setprio 0
	s_setprio 1
	v_mfma_f32_16x16x128_f8f6f4 v[128:131], v[10:17], v[202:209], 0
	v_mfma_f32_16x16x128_f8f6f4 v[124:127], v[2:9], v[202:209], 0
	v_mfma_f32_16x16x128_f8f6f4 v[120:123], v[10:17], v[222:229], 0
	v_mfma_f32_16x16x128_f8f6f4 v[116:119], v[2:9], v[222:229], 0
	v_mfma_f32_16x16x128_f8f6f4 v[112:115], v[10:17], v[230:237], 0
	v_mfma_f32_16x16x128_f8f6f4 v[108:111], v[2:9], v[230:237], 0
	v_mfma_f32_16x16x128_f8f6f4 v[104:107], v[10:17], v[238:245], 0
	v_mfma_f32_16x16x128_f8f6f4 v[100:103], v[2:9], v[238:245], 0
	s_setprio 0
	s_barrier
	s_add_i32 s52, s52, s68
	v_lshl_add_u64 v[194:195], s[30:31], 0, v[170:171]
	s_add_i32 s85, s52, 0x2000
	v_lshl_add_u64 v[178:179], v[194:195], 0, s[28:29]
	s_mov_b32 m0, s52
	v_lshl_add_u64 v[196:197], s[30:31], 0, v[172:173]
	s_add_u32 s36, s30, 0x20100
	ds_read_b128 v[202:205], v169 offset:16384
	ds_read_b128 v[206:209], v169 offset:17408
	ds_read_b128 v[222:225], v169 offset:18432
	ds_read_b128 v[226:229], v169 offset:19456
	ds_read_b128 v[230:233], v169 offset:20480
	ds_read_b128 v[234:237], v169 offset:21504
	ds_read_b128 v[238:241], v169 offset:22528
	ds_read_b128 v[242:245], v169 offset:23552
	global_load_lds_dwordx4 v[178:179], off
	v_lshl_add_u64 v[178:179], v[196:197], 0, s[28:29]
	s_mov_b32 m0, s85
	s_addc_u32 s37, s31, 0
	s_add_i32 s55, s55, s68
	global_load_lds_dwordx4 v[178:179], off
	v_lshl_add_u64 v[178:179], s[36:37], 0, v[170:171]
	s_mov_b32 m0, s55
	s_add_i32 s65, s55, 0x2000
	global_load_lds_dwordx4 v[178:179], off
	v_lshl_add_u64 v[178:179], s[36:37], 0, v[172:173]
	s_mov_b32 m0, s65
	v_readlane_b32 s26, v253, 37
	global_load_lds_dwordx4 v[178:179], off
	s_mov_b32 m0, s69
	v_readlane_b32 s27, v253, 38
	s_nop 4
	global_load_lds_dwordx4 v34, s[26:27]
	s_mov_b32 m0, s70
	s_nop 0
	global_load_lds_dwordx4 v192, s[26:27]
	s_waitcnt vmcnt(8)
	s_waitcnt lgkmcnt(0)
	s_barrier
	s_setprio 1
	s_waitcnt lgkmcnt(0)
	v_mfma_f32_16x16x128_f8f6f4 v[96:99], v[26:33], v[202:209], 0
	v_mfma_f32_16x16x128_f8f6f4 v[92:95], v[18:25], v[202:209], 0
	v_mfma_f32_16x16x128_f8f6f4 v[88:91], v[26:33], v[222:229], 0
	v_mfma_f32_16x16x128_f8f6f4 v[84:87], v[18:25], v[222:229], 0
	v_mfma_f32_16x16x128_f8f6f4 v[80:83], v[26:33], v[230:237], 0
	v_mfma_f32_16x16x128_f8f6f4 v[76:79], v[18:25], v[230:237], 0
	v_mfma_f32_16x16x128_f8f6f4 v[72:75], v[26:33], v[238:245], 0
	v_mfma_f32_16x16x128_f8f6f4 v[68:71], v[18:25], v[238:245], 0
	s_setprio 0
	s_setprio 1
	v_mfma_f32_16x16x128_f8f6f4 v[64:67], v[10:17], v[202:209], 0
	v_mfma_f32_16x16x128_f8f6f4 v[60:63], v[2:9], v[202:209], 0
	v_mfma_f32_16x16x128_f8f6f4 v[56:59], v[10:17], v[222:229], 0
	v_mfma_f32_16x16x128_f8f6f4 v[52:55], v[2:9], v[222:229], 0
	v_mfma_f32_16x16x128_f8f6f4 v[48:51], v[10:17], v[230:237], 0
	v_mfma_f32_16x16x128_f8f6f4 v[44:47], v[2:9], v[230:237], 0
	v_mfma_f32_16x16x128_f8f6f4 v[40:43], v[10:17], v[238:245], 0
	v_mfma_f32_16x16x128_f8f6f4 v[36:39], v[2:9], v[238:245], 0
	s_setprio 0
	s_barrier
	s_add_i32 s54, 0, 0x18000
	s_add_i32 s51, 0, 0x1c000
	v_add_u32_e32 v201, s54, v167
	v_add_u32_e32 v202, s51, v167
	ds_read_b128 v[26:29], v201
	ds_read_b128 v[30:33], v201 offset:1024
	ds_read_b128 v[18:21], v201 offset:2048
	ds_read_b128 v[22:25], v201 offset:3072
	ds_read_b128 v[10:13], v202
	ds_read_b128 v[14:17], v202 offset:1024
	ds_read_b128 v[2:5], v202 offset:2048
	ds_read_b128 v[6:9], v202 offset:3072
	s_mov_b32 m0, s71
	ds_read_b128 v[204:207], v169 offset:32768
	ds_read_b128 v[208:211], v169 offset:33792
	ds_read_b128 v[222:225], v169 offset:34816
	ds_read_b128 v[226:229], v169 offset:35840
	ds_read_b128 v[230:233], v169 offset:36864
	ds_read_b128 v[234:237], v169 offset:37888
	ds_read_b128 v[238:241], v169 offset:38912
	ds_read_b128 v[242:245], v169 offset:39936
	global_load_lds_dwordx4 v189, s[26:27]
	s_mov_b32 m0, s72
	s_nop 0
	global_load_lds_dwordx4 v198, s[26:27]
	s_waitcnt vmcnt(8)
	s_waitcnt lgkmcnt(0)
	s_barrier
	s_setprio 1
	s_waitcnt lgkmcnt(0)
	v_mfma_f32_16x16x128_f8f6f4 v[160:163], v[26:33], v[204:211], v[160:163]
	v_mfma_f32_16x16x128_f8f6f4 v[156:159], v[18:25], v[204:211], v[156:159]
	v_mfma_f32_16x16x128_f8f6f4 v[152:155], v[26:33], v[222:229], v[152:155]
	v_mfma_f32_16x16x128_f8f6f4 v[148:151], v[18:25], v[222:229], v[148:151]
	v_mfma_f32_16x16x128_f8f6f4 v[144:147], v[26:33], v[230:237], v[144:147]
	v_mfma_f32_16x16x128_f8f6f4 v[140:143], v[18:25], v[230:237], v[140:143]
	v_mfma_f32_16x16x128_f8f6f4 v[136:139], v[26:33], v[238:245], v[136:139]
	v_mfma_f32_16x16x128_f8f6f4 v[132:135], v[18:25], v[238:245], v[132:135]
	s_setprio 0
	s_setprio 1
	v_mfma_f32_16x16x128_f8f6f4 v[128:131], v[10:17], v[204:211], v[128:131]
	v_mfma_f32_16x16x128_f8f6f4 v[124:127], v[2:9], v[204:211], v[124:127]
	v_mfma_f32_16x16x128_f8f6f4 v[120:123], v[10:17], v[222:229], v[120:123]
	v_mfma_f32_16x16x128_f8f6f4 v[116:119], v[2:9], v[222:229], v[116:119]
	v_mfma_f32_16x16x128_f8f6f4 v[112:115], v[10:17], v[230:237], v[112:115]
	v_mfma_f32_16x16x128_f8f6f4 v[108:111], v[2:9], v[230:237], v[108:111]
	v_mfma_f32_16x16x128_f8f6f4 v[104:107], v[10:17], v[238:245], v[104:107]
	v_mfma_f32_16x16x128_f8f6f4 v[100:103], v[2:9], v[238:245], v[100:103]
	s_setprio 0
	s_barrier
	s_add_i32 s54, s54, s68
	s_mov_b64 s[26:27], 0x180
	s_add_i32 s50, s54, 0x2000
	v_lshl_add_u64 v[178:179], v[194:195], 0, s[26:27]
	s_mov_b32 m0, s54
	s_add_u32 s30, s30, 0x20180
	ds_read_b128 v[204:207], v169 offset:49152
	ds_read_b128 v[208:211], v169 offset:50176
	ds_read_b128 v[222:225], v169 offset:51200
	ds_read_b128 v[226:229], v169 offset:52224
	ds_read_b128 v[230:233], v169 offset:53248
	ds_read_b128 v[234:237], v169 offset:54272
	ds_read_b128 v[238:241], v169 offset:55296
	ds_read_b128 v[242:245], v169 offset:56320
	global_load_lds_dwordx4 v[178:179], off
	v_lshl_add_u64 v[178:179], v[196:197], 0, s[26:27]
	s_mov_b32 m0, s50
	s_addc_u32 s31, s31, 0
	s_add_i32 s51, s51, s68
	global_load_lds_dwordx4 v[178:179], off
	v_lshl_add_u64 v[178:179], s[30:31], 0, v[170:171]
	s_mov_b32 m0, s51
	s_add_i32 s64, s51, 0x2000
	global_load_lds_dwordx4 v[178:179], off
	v_lshl_add_u64 v[178:179], s[30:31], 0, v[172:173]
	s_mov_b32 m0, s64
	v_readlane_b32 s26, v253, 39
	global_load_lds_dwordx4 v[178:179], off
	s_mov_b32 m0, s75
	v_readlane_b32 s27, v253, 40
	s_nop 4
	global_load_lds_dwordx4 v34, s[26:27]
	s_mov_b32 m0, s76
	s_nop 0
	global_load_lds_dwordx4 v192, s[26:27]
	s_waitcnt vmcnt(8)
	s_waitcnt lgkmcnt(0)
	s_barrier
	s_setprio 1
	s_waitcnt lgkmcnt(0)
	v_mfma_f32_16x16x128_f8f6f4 v[96:99], v[26:33], v[204:211], v[96:99]
	v_mfma_f32_16x16x128_f8f6f4 v[92:95], v[18:25], v[204:211], v[92:95]
	v_mfma_f32_16x16x128_f8f6f4 v[88:91], v[26:33], v[222:229], v[88:91]
	v_mfma_f32_16x16x128_f8f6f4 v[84:87], v[18:25], v[222:229], v[84:87]
	v_mfma_f32_16x16x128_f8f6f4 v[80:83], v[26:33], v[230:237], v[80:83]
	v_mfma_f32_16x16x128_f8f6f4 v[76:79], v[18:25], v[230:237], v[76:79]
	v_mfma_f32_16x16x128_f8f6f4 v[72:75], v[26:33], v[238:245], v[72:75]
	v_mfma_f32_16x16x128_f8f6f4 v[68:71], v[18:25], v[238:245], v[68:71]
	s_setprio 0
	s_setprio 1
	v_mfma_f32_16x16x128_f8f6f4 v[64:67], v[10:17], v[204:211], v[64:67]
	v_mfma_f32_16x16x128_f8f6f4 v[60:63], v[2:9], v[204:211], v[60:63]
	v_mfma_f32_16x16x128_f8f6f4 v[56:59], v[10:17], v[222:229], v[56:59]
	v_mfma_f32_16x16x128_f8f6f4 v[52:55], v[2:9], v[222:229], v[52:55]
	v_mfma_f32_16x16x128_f8f6f4 v[48:51], v[10:17], v[230:237], v[48:51]
	v_mfma_f32_16x16x128_f8f6f4 v[44:47], v[2:9], v[230:237], v[44:47]
	v_mfma_f32_16x16x128_f8f6f4 v[40:43], v[10:17], v[238:245], v[40:43]
	v_mfma_f32_16x16x128_f8f6f4 v[36:39], v[2:9], v[238:245], v[36:39]
	s_setprio 0
	s_barrier
	v_lshl_add_u64 v[18:19], s[26:27], 0, v[174:175]
	v_lshl_add_u64 v[20:21], s[26:27], 0, v[190:191]
	s_mov_b32 s63, 0
	s_mov_b64 s[30:31], 0
	s_branch .LBB0_821
	.p2align	6

.LBB0_899:
	s_mul_i32 s14, s81, 0xe0000
	s_add_u32 s40, s44, s14
	s_addc_u32 s41, s45, 0
	s_and_b64 s[6:7], s[6:7], exec
	s_cselect_b32 s52, s41, s43
	s_cselect_b32 s53, s40, s42
	s_add_i32 s54, 0, 0x10000
	s_add_i32 s65, 0, 0x14000
	v_add_u32_e32 v34, s54, v167
	v_add_u32_e32 v206, s65, v167
	ds_read_b128 v[26:29], v34
	ds_read_b128 v[30:33], v34 offset:1024
	ds_read_b128 v[18:21], v34 offset:2048
	ds_read_b128 v[22:25], v34 offset:3072
	ds_read_b128 v[10:13], v206
	ds_read_b128 v[14:17], v206 offset:1024
	ds_read_b128 v[2:5], v206 offset:2048
	ds_read_b128 v[6:9], v206 offset:3072
	s_add_u32 s6, s42, 0x70080
	s_addc_u32 s7, s43, 0
	s_add_i32 s84, s72, 0xc000
	v_lshl_add_u64 v[216:217], s[6:7], 0, v[174:175]
	s_mov_b32 m0, s84
	s_add_i32 s85, s72, 0xe000
	ds_read_b128 v[178:181], v189
	ds_read_b128 v[182:185], v189 offset:1024
	ds_read_b128 v[198:201], v189 offset:2048
	ds_read_b128 v[202:205], v189 offset:3072
	ds_read_b128 v[208:211], v189 offset:4096
	ds_read_b128 v[212:215], v189 offset:5120
	ds_read_b128 v[222:225], v189 offset:6144
	ds_read_b128 v[226:229], v189 offset:7168
	global_load_lds_dwordx4 v[216:217], off
	v_lshl_add_u64 v[216:217], s[6:7], 0, v[170:171]
	s_mov_b32 m0, s85
	s_nop 0
	global_load_lds_dwordx4 v[216:217], off
	s_waitcnt vmcnt(8)
	s_waitcnt lgkmcnt(0)
	s_barrier
	s_setprio 1
	s_waitcnt lgkmcnt(0)
	v_mfma_f32_16x16x128_f8f6f4 v[160:163], v[26:33], v[178:185], 0
	v_mfma_f32_16x16x128_f8f6f4 v[156:159], v[18:25], v[178:185], 0
	v_mfma_f32_16x16x128_f8f6f4 v[152:155], v[26:33], v[198:205], 0
	v_mfma_f32_16x16x128_f8f6f4 v[148:151], v[18:25], v[198:205], 0
	v_mfma_f32_16x16x128_f8f6f4 v[144:147], v[26:33], v[208:215], 0
	v_mfma_f32_16x16x128_f8f6f4 v[140:143], v[18:25], v[208:215], 0
	v_mfma_f32_16x16x128_f8f6f4 v[136:139], v[26:33], v[222:229], 0
	v_mfma_f32_16x16x128_f8f6f4 v[132:135], v[18:25], v[222:229], 0
	s_setprio 0
	s_setprio 1
	v_mfma_f32_16x16x128_f8f6f4 v[128:131], v[10:17], v[178:185], 0
	v_mfma_f32_16x16x128_f8f6f4 v[124:127], v[2:9], v[178:185], 0
	v_mfma_f32_16x16x128_f8f6f4 v[120:123], v[10:17], v[198:205], 0
	v_mfma_f32_16x16x128_f8f6f4 v[116:119], v[2:9], v[198:205], 0
	v_mfma_f32_16x16x128_f8f6f4 v[112:115], v[10:17], v[208:215], 0
	v_mfma_f32_16x16x128_f8f6f4 v[108:111], v[2:9], v[208:215], 0
	v_mfma_f32_16x16x128_f8f6f4 v[104:107], v[10:17], v[222:229], 0
	v_mfma_f32_16x16x128_f8f6f4 v[100:103], v[2:9], v[222:229], 0
	s_setprio 0
	s_barrier
	v_lshl_add_u64 v[198:199], v[196:197], 0, v[172:173]
	s_add_i32 s54, s54, s71
	v_lshl_add_u64 v[200:201], v[198:199], 0, s[28:29]
	s_mov_b32 m0, s54
	ds_read_b128 v[178:181], v189 offset:16384
	ds_read_b128 v[182:185], v189 offset:17408
	ds_read_b128 v[208:211], v189 offset:18432
	ds_read_b128 v[212:215], v189 offset:19456
	ds_read_b128 v[222:225], v189 offset:20480
	ds_read_b128 v[226:229], v189 offset:21504
	ds_read_b128 v[230:233], v189 offset:22528
	ds_read_b128 v[234:237], v189 offset:23552
	global_load_lds_dwordx4 v[200:201], off
	v_lshl_add_u64 v[200:201], v[196:197], 0, v[168:169]
	s_add_i32 s55, s54, 0x2000
	v_lshl_add_u64 v[202:203], v[200:201], 0, s[28:29]
	s_mov_b32 m0, s55
	s_mov_b64 s[6:7], 0x70100
	global_load_lds_dwordx4 v[202:203], off
	v_lshl_add_u64 v[202:203], v[196:197], 0, s[6:7]
	s_add_i32 s65, s65, s71
	v_lshl_add_u64 v[204:205], v[202:203], 0, v[172:173]
	s_mov_b32 m0, s65
	s_add_i32 s67, s65, 0x2000
	global_load_lds_dwordx4 v[204:205], off
	v_lshl_add_u64 v[202:203], v[202:203], 0, v[168:169]
	s_mov_b32 m0, s67
	s_nop 0
	global_load_lds_dwordx4 v[202:203], off
	v_lshl_add_u64 v[202:203], s[42:43], 0, v[174:175]
	v_lshl_add_u64 v[204:205], v[202:203], 0, s[28:29]
	s_mov_b32 m0, s72
	s_nop 0
	global_load_lds_dwordx4 v[204:205], off
	v_lshl_add_u64 v[204:205], s[42:43], 0, v[170:171]
	v_lshl_add_u64 v[216:217], v[204:205], 0, s[28:29]
	s_mov_b32 m0, s73
	s_nop 0
	global_load_lds_dwordx4 v[216:217], off
	s_waitcnt vmcnt(8)
	s_waitcnt lgkmcnt(0)
	s_barrier
	s_setprio 1
	s_waitcnt lgkmcnt(0)
	v_mfma_f32_16x16x128_f8f6f4 v[96:99], v[26:33], v[178:185], 0
	v_mfma_f32_16x16x128_f8f6f4 v[92:95], v[18:25], v[178:185], 0
	v_mfma_f32_16x16x128_f8f6f4 v[88:91], v[26:33], v[208:215], 0
	v_mfma_f32_16x16x128_f8f6f4 v[84:87], v[18:25], v[208:215], 0
	v_mfma_f32_16x16x128_f8f6f4 v[80:83], v[26:33], v[222:229], 0
	v_mfma_f32_16x16x128_f8f6f4 v[76:79], v[18:25], v[222:229], 0
	v_mfma_f32_16x16x128_f8f6f4 v[72:75], v[26:33], v[230:237], 0
	v_mfma_f32_16x16x128_f8f6f4 v[68:71], v[18:25], v[230:237], 0
	s_setprio 0
	s_setprio 1
	v_mfma_f32_16x16x128_f8f6f4 v[64:67], v[10:17], v[178:185], 0
	v_mfma_f32_16x16x128_f8f6f4 v[60:63], v[2:9], v[178:185], 0
	v_mfma_f32_16x16x128_f8f6f4 v[56:59], v[10:17], v[208:215], 0
	v_mfma_f32_16x16x128_f8f6f4 v[52:55], v[2:9], v[208:215], 0
	v_mfma_f32_16x16x128_f8f6f4 v[48:51], v[10:17], v[222:229], 0
	v_mfma_f32_16x16x128_f8f6f4 v[44:47], v[2:9], v[222:229], 0
	v_mfma_f32_16x16x128_f8f6f4 v[40:43], v[10:17], v[230:237], 0
	v_mfma_f32_16x16x128_f8f6f4 v[36:39], v[2:9], v[230:237], 0
	s_setprio 0
	s_barrier
	s_add_i32 s50, 0, 0x18000
	s_add_i32 s63, 0, 0x1c000
	v_add_u32_e32 v207, s50, v167
	v_add_u32_e32 v208, s63, v167
	ds_read_b128 v[26:29], v207
	ds_read_b128 v[30:33], v207 offset:1024
	ds_read_b128 v[18:21], v207 offset:2048
	ds_read_b128 v[22:25], v207 offset:3072
	ds_read_b128 v[10:13], v208
	ds_read_b128 v[14:17], v208 offset:1024
	ds_read_b128 v[2:5], v208 offset:2048
	ds_read_b128 v[6:9], v208 offset:3072
	s_add_u32 s6, s42, 0x70100
	s_addc_u32 s7, s43, 0
	s_mov_b32 m0, s74
	v_lshl_add_u64 v[218:219], s[6:7], 0, v[174:175]
	ds_read_b128 v[178:181], v189 offset:32768
	ds_read_b128 v[182:185], v189 offset:33792
	ds_read_b128 v[210:213], v189 offset:34816
	ds_read_b128 v[214:217], v189 offset:35840
	ds_read_b128 v[222:225], v189 offset:36864
	ds_read_b128 v[226:229], v189 offset:37888
	ds_read_b128 v[230:233], v189 offset:38912
	ds_read_b128 v[234:237], v189 offset:39936
	global_load_lds_dwordx4 v[218:219], off
	v_lshl_add_u64 v[218:219], s[6:7], 0, v[170:171]
	s_mov_b32 m0, s75
	s_nop 0
	global_load_lds_dwordx4 v[218:219], off
	s_waitcnt vmcnt(8)
	s_waitcnt lgkmcnt(0)
	s_barrier
	s_setprio 1
	s_waitcnt lgkmcnt(0)
	v_mfma_f32_16x16x128_f8f6f4 v[160:163], v[26:33], v[178:185], v[160:163]
	v_mfma_f32_16x16x128_f8f6f4 v[156:159], v[18:25], v[178:185], v[156:159]
	v_mfma_f32_16x16x128_f8f6f4 v[152:155], v[26:33], v[210:217], v[152:155]
	v_mfma_f32_16x16x128_f8f6f4 v[148:151], v[18:25], v[210:217], v[148:151]
	v_mfma_f32_16x16x128_f8f6f4 v[144:147], v[26:33], v[222:229], v[144:147]
	v_mfma_f32_16x16x128_f8f6f4 v[140:143], v[18:25], v[222:229], v[140:143]
	v_mfma_f32_16x16x128_f8f6f4 v[136:139], v[26:33], v[230:237], v[136:139]
	v_mfma_f32_16x16x128_f8f6f4 v[132:135], v[18:25], v[230:237], v[132:135]
	s_setprio 0
	s_setprio 1
	v_mfma_f32_16x16x128_f8f6f4 v[128:131], v[10:17], v[178:185], v[128:131]
	v_mfma_f32_16x16x128_f8f6f4 v[124:127], v[2:9], v[178:185], v[124:127]
	v_mfma_f32_16x16x128_f8f6f4 v[120:123], v[10:17], v[210:217], v[120:123]
	v_mfma_f32_16x16x128_f8f6f4 v[116:119], v[2:9], v[210:217], v[116:119]
	v_mfma_f32_16x16x128_f8f6f4 v[112:115], v[10:17], v[222:229], v[112:115]
	v_mfma_f32_16x16x128_f8f6f4 v[108:111], v[2:9], v[222:229], v[108:111]
	v_mfma_f32_16x16x128_f8f6f4 v[104:107], v[10:17], v[230:237], v[104:107]
	v_mfma_f32_16x16x128_f8f6f4 v[100:103], v[2:9], v[230:237], v[100:103]
	s_setprio 0
	s_barrier
	s_mov_b64 s[6:7], 0x180
	s_add_i32 s50, s50, s71
	v_lshl_add_u64 v[198:199], v[198:199], 0, s[6:7]
	s_mov_b32 m0, s50
	s_add_i32 s51, s50, 0x2000
	ds_read_b128 v[178:181], v189 offset:49152
	ds_read_b128 v[182:185], v189 offset:50176
	ds_read_b128 v[210:213], v189 offset:51200
	ds_read_b128 v[214:217], v189 offset:52224
	ds_read_b128 v[222:225], v189 offset:53248
	ds_read_b128 v[226:229], v189 offset:54272
	ds_read_b128 v[230:233], v189 offset:55296
	ds_read_b128 v[234:237], v189 offset:56320
	global_load_lds_dwordx4 v[198:199], off
	v_lshl_add_u64 v[198:199], v[200:201], 0, s[6:7]
	s_mov_b32 m0, s51
	s_add_i32 s63, s63, s71
	global_load_lds_dwordx4 v[198:199], off
	v_lshl_add_u64 v[198:199], v[196:197], 0, s[26:27]
	v_lshl_add_u64 v[200:201], v[198:199], 0, v[172:173]
	s_mov_b32 m0, s63
	s_add_i32 s64, s63, 0x2000
	global_load_lds_dwordx4 v[200:201], off
	v_lshl_add_u64 v[198:199], v[198:199], 0, v[168:169]
	s_mov_b32 m0, s64
	s_nop 0
	global_load_lds_dwordx4 v[198:199], off
	v_lshl_add_u64 v[198:199], v[202:203], 0, s[6:7]
	s_mov_b32 m0, s77
	s_nop 0
	global_load_lds_dwordx4 v[198:199], off
	v_lshl_add_u64 v[198:199], v[204:205], 0, s[6:7]
	s_mov_b32 m0, s78
	s_nop 0
	global_load_lds_dwordx4 v[198:199], off
	s_waitcnt vmcnt(8)
	s_waitcnt lgkmcnt(0)
	s_barrier
	s_setprio 1
	s_waitcnt lgkmcnt(0)
	v_mfma_f32_16x16x128_f8f6f4 v[96:99], v[26:33], v[178:185], v[96:99]
	v_mfma_f32_16x16x128_f8f6f4 v[92:95], v[18:25], v[178:185], v[92:95]
	v_mfma_f32_16x16x128_f8f6f4 v[88:91], v[26:33], v[210:217], v[88:91]
	v_mfma_f32_16x16x128_f8f6f4 v[84:87], v[18:25], v[210:217], v[84:87]
	v_mfma_f32_16x16x128_f8f6f4 v[80:83], v[26:33], v[222:229], v[80:83]
	v_mfma_f32_16x16x128_f8f6f4 v[76:79], v[18:25], v[222:229], v[76:79]
	v_mfma_f32_16x16x128_f8f6f4 v[72:75], v[26:33], v[230:237], v[72:75]
	v_mfma_f32_16x16x128_f8f6f4 v[68:71], v[18:25], v[230:237], v[68:71]
	s_setprio 0
	s_setprio 1
	v_mfma_f32_16x16x128_f8f6f4 v[64:67], v[10:17], v[178:185], v[64:67]
	v_mfma_f32_16x16x128_f8f6f4 v[60:63], v[2:9], v[178:185], v[60:63]
	v_mfma_f32_16x16x128_f8f6f4 v[56:59], v[10:17], v[210:217], v[56:59]
	v_mfma_f32_16x16x128_f8f6f4 v[52:55], v[2:9], v[210:217], v[52:55]
	v_mfma_f32_16x16x128_f8f6f4 v[48:51], v[10:17], v[222:229], v[48:51]
	v_mfma_f32_16x16x128_f8f6f4 v[44:47], v[2:9], v[222:229], v[44:47]
	v_mfma_f32_16x16x128_f8f6f4 v[40:43], v[10:17], v[230:237], v[40:43]
	v_mfma_f32_16x16x128_f8f6f4 v[36:39], v[2:9], v[230:237], v[36:39]
	s_setprio 0
	s_barrier
	s_mov_b64 s[6:7], 0x200
	v_lshl_add_u64 v[18:19], v[196:197], 0, s[6:7]
	s_mov_b32 s86, 0
	.p2align	6

.LBB0_953:
	s_add_u32 s95, s30, 0x200
	s_addc_u32 s96, s31, 0
	s_add_i32 s65, 0, 0x14000
	s_add_i32 s67, 0, 0x10000
	v_add_u32_e32 v199, s65, v167
	v_add_u32_e32 v200, s67, v167
	ds_read_b128 v[10:13], v199
	ds_read_b128 v[14:17], v199 offset:1024
	ds_read_b128 v[2:5], v199 offset:2048
	ds_read_b128 v[6:9], v199 offset:3072
	ds_read_b128 v[22:25], v200 offset:3072
	ds_read_b128 v[18:21], v200 offset:2048
	ds_read_b128 v[30:33], v200 offset:1024
	ds_read_b128 v[26:29], v200
	s_lshl_b32 s14, s94, 10
	s_add_i32 s97, s14, 0
	s_add_i32 s97, s97, 0x20400
	v_mov_b32_e32 v191, v35
	v_mov_b32_e32 v175, v35
	s_add_i32 s83, s52, 0xc000
	v_readlane_b32 s26, v253, 28
	s_mov_b32 m0, s83
	v_readlane_b32 s27, v253, 29
	s_add_i32 s53, s52, 0xe000
	ds_read_b128 v[178:181], v169
	ds_read_b128 v[182:185], v169 offset:1024
	ds_read_b128 v[202:205], v169 offset:2048
	ds_read_b128 v[206:209], v169 offset:3072
	ds_read_b128 v[210:213], v169 offset:4096
	ds_read_b128 v[214:217], v169 offset:5120
	ds_read_b128 v[222:225], v169 offset:6144
	ds_read_b128 v[226:229], v169 offset:7168
	global_load_lds_dwordx4 v190, s[26:27]
	s_mov_b32 m0, s53
	s_nop 0
	global_load_lds_dwordx4 v174, s[26:27]
	s_waitcnt vmcnt(8)
	s_waitcnt lgkmcnt(0)
	s_barrier
	s_setprio 1
	s_waitcnt lgkmcnt(0)
	v_mfma_f32_16x16x128_f8f6f4 v[160:163], v[26:33], v[178:185], 0
	v_mfma_f32_16x16x128_f8f6f4 v[156:159], v[18:25], v[178:185], 0
	v_mfma_f32_16x16x128_f8f6f4 v[152:155], v[26:33], v[202:209], 0
	v_mfma_f32_16x16x128_f8f6f4 v[148:151], v[18:25], v[202:209], 0
	v_mfma_f32_16x16x128_f8f6f4 v[144:147], v[26:33], v[210:217], 0
	v_mfma_f32_16x16x128_f8f6f4 v[140:143], v[18:25], v[210:217], 0
	v_mfma_f32_16x16x128_f8f6f4 v[136:139], v[26:33], v[222:229], 0
	v_mfma_f32_16x16x128_f8f6f4 v[132:135], v[18:25], v[222:229], 0
	s_setprio 0
	s_setprio 1
	v_mfma_f32_16x16x128_f8f6f4 v[128:131], v[10:17], v[178:185], 0
	v_mfma_f32_16x16x128_f8f6f4 v[124:127], v[2:9], v[178:185], 0
	v_mfma_f32_16x16x128_f8f6f4 v[120:123], v[10:17], v[202:209], 0
	v_mfma_f32_16x16x128_f8f6f4 v[116:119], v[2:9], v[202:209], 0
	v_mfma_f32_16x16x128_f8f6f4 v[112:115], v[10:17], v[210:217], 0
	v_mfma_f32_16x16x128_f8f6f4 v[108:111], v[2:9], v[210:217], 0
	v_mfma_f32_16x16x128_f8f6f4 v[104:107], v[10:17], v[222:229], 0
	v_mfma_f32_16x16x128_f8f6f4 v[100:103], v[2:9], v[222:229], 0
	s_setprio 0
	s_barrier
	v_lshl_add_u64 v[194:195], s[30:31], 0, v[170:171]
	s_add_i32 s67, s67, s82
	v_lshl_add_u64 v[196:197], v[194:195], 0, s[28:29]
	s_mov_b32 m0, s67
	s_add_i32 s55, s67, 0x2000
	ds_read_b128 v[178:181], v169 offset:16384
	ds_read_b128 v[182:185], v169 offset:17408
	ds_read_b128 v[202:205], v169 offset:18432
	ds_read_b128 v[206:209], v169 offset:19456
	ds_read_b128 v[210:213], v169 offset:20480
	ds_read_b128 v[214:217], v169 offset:21504
	ds_read_b128 v[222:225], v169 offset:22528
	ds_read_b128 v[226:229], v169 offset:23552
	global_load_lds_dwordx4 v[196:197], off
	v_lshl_add_u64 v[196:197], s[30:31], 0, v[172:173]
	s_add_u32 s46, s30, 0x20100
	v_lshl_add_u64 v[218:219], v[196:197], 0, s[28:29]
	s_mov_b32 m0, s55
	s_addc_u32 s47, s31, 0
	s_add_i32 s65, s65, s82
	global_load_lds_dwordx4 v[218:219], off
	v_lshl_add_u64 v[218:219], s[46:47], 0, v[170:171]
	s_mov_b32 m0, s65
	s_add_i32 s54, s65, 0x2000
	global_load_lds_dwordx4 v[218:219], off
	v_lshl_add_u64 v[218:219], s[46:47], 0, v[172:173]
	s_mov_b32 m0, s54
	v_readlane_b32 s26, v253, 37
	global_load_lds_dwordx4 v[218:219], off
	s_mov_b32 m0, s52
	v_readlane_b32 s27, v253, 38
	s_nop 4
	global_load_lds_dwordx4 v34, s[26:27]
	s_mov_b32 m0, s84
	s_nop 0
	global_load_lds_dwordx4 v192, s[26:27]
	s_waitcnt vmcnt(8)
	s_waitcnt lgkmcnt(0)
	s_barrier
	s_setprio 1
	s_waitcnt lgkmcnt(0)
	v_mfma_f32_16x16x128_f8f6f4 v[96:99], v[26:33], v[178:185], 0
	v_mfma_f32_16x16x128_f8f6f4 v[92:95], v[18:25], v[178:185], 0
	v_mfma_f32_16x16x128_f8f6f4 v[88:91], v[26:33], v[202:209], 0
	v_mfma_f32_16x16x128_f8f6f4 v[84:87], v[18:25], v[202:209], 0
	v_mfma_f32_16x16x128_f8f6f4 v[80:83], v[26:33], v[210:217], 0
	v_mfma_f32_16x16x128_f8f6f4 v[76:79], v[18:25], v[210:217], 0
	v_mfma_f32_16x16x128_f8f6f4 v[72:75], v[26:33], v[222:229], 0
	v_mfma_f32_16x16x128_f8f6f4 v[68:71], v[18:25], v[222:229], 0
	s_setprio 0
	s_setprio 1
	v_mfma_f32_16x16x128_f8f6f4 v[64:67], v[10:17], v[178:185], 0
	v_mfma_f32_16x16x128_f8f6f4 v[60:63], v[2:9], v[178:185], 0
	v_mfma_f32_16x16x128_f8f6f4 v[56:59], v[10:17], v[202:209], 0
	v_mfma_f32_16x16x128_f8f6f4 v[52:55], v[2:9], v[202:209], 0
	v_mfma_f32_16x16x128_f8f6f4 v[48:51], v[10:17], v[210:217], 0
	v_mfma_f32_16x16x128_f8f6f4 v[44:47], v[2:9], v[210:217], 0
	v_mfma_f32_16x16x128_f8f6f4 v[40:43], v[10:17], v[222:229], 0
	v_mfma_f32_16x16x128_f8f6f4 v[36:39], v[2:9], v[222:229], 0
	s_setprio 0
	s_barrier
	s_add_i32 s50, 0, 0x18000
	s_add_i32 s64, 0, 0x1c000
	v_add_u32_e32 v201, s50, v167
	v_add_u32_e32 v202, s64, v167
	ds_read_b128 v[26:29], v201
	ds_read_b128 v[30:33], v201 offset:1024
	ds_read_b128 v[18:21], v201 offset:2048
	ds_read_b128 v[22:25], v201 offset:3072
	ds_read_b128 v[10:13], v202
	ds_read_b128 v[14:17], v202 offset:1024
	ds_read_b128 v[2:5], v202 offset:2048
	ds_read_b128 v[6:9], v202 offset:3072
	s_mov_b32 m0, s85
	ds_read_b128 v[178:181], v169 offset:32768
	ds_read_b128 v[182:185], v169 offset:33792
	ds_read_b128 v[204:207], v169 offset:34816
	ds_read_b128 v[208:211], v169 offset:35840
	ds_read_b128 v[212:215], v169 offset:36864
	ds_read_b128 v[216:219], v169 offset:37888
	ds_read_b128 v[222:225], v169 offset:38912
	ds_read_b128 v[226:229], v169 offset:39936
	global_load_lds_dwordx4 v189, s[26:27]
	s_mov_b32 m0, s86
	s_nop 0
	global_load_lds_dwordx4 v198, s[26:27]
	s_waitcnt vmcnt(8)
	s_waitcnt lgkmcnt(0)
	s_barrier
	s_setprio 1
	s_waitcnt lgkmcnt(0)
	v_mfma_f32_16x16x128_f8f6f4 v[160:163], v[26:33], v[178:185], v[160:163]
	v_mfma_f32_16x16x128_f8f6f4 v[156:159], v[18:25], v[178:185], v[156:159]
	v_mfma_f32_16x16x128_f8f6f4 v[152:155], v[26:33], v[204:211], v[152:155]
	v_mfma_f32_16x16x128_f8f6f4 v[148:151], v[18:25], v[204:211], v[148:151]
	v_mfma_f32_16x16x128_f8f6f4 v[144:147], v[26:33], v[212:219], v[144:147]
	v_mfma_f32_16x16x128_f8f6f4 v[140:143], v[18:25], v[212:219], v[140:143]
	v_mfma_f32_16x16x128_f8f6f4 v[136:139], v[26:33], v[222:229], v[136:139]
	v_mfma_f32_16x16x128_f8f6f4 v[132:135], v[18:25], v[222:229], v[132:135]
	s_setprio 0
	s_setprio 1
	v_mfma_f32_16x16x128_f8f6f4 v[128:131], v[10:17], v[178:185], v[128:131]
	v_mfma_f32_16x16x128_f8f6f4 v[124:127], v[2:9], v[178:185], v[124:127]
	v_mfma_f32_16x16x128_f8f6f4 v[120:123], v[10:17], v[204:211], v[120:123]
	v_mfma_f32_16x16x128_f8f6f4 v[116:119], v[2:9], v[204:211], v[116:119]
	v_mfma_f32_16x16x128_f8f6f4 v[112:115], v[10:17], v[212:219], v[112:115]
	v_mfma_f32_16x16x128_f8f6f4 v[108:111], v[2:9], v[212:219], v[108:111]
	v_mfma_f32_16x16x128_f8f6f4 v[104:107], v[10:17], v[222:229], v[104:107]
	v_mfma_f32_16x16x128_f8f6f4 v[100:103], v[2:9], v[222:229], v[100:103]
	s_setprio 0
	s_barrier
	s_add_i32 s50, s50, s82
	s_mov_b64 s[26:27], 0x180
	s_add_i32 s51, s50, 0x2000
	v_lshl_add_u64 v[194:195], v[194:195], 0, s[26:27]
	s_mov_b32 m0, s50
	s_add_u32 s30, s30, 0x20180
	ds_read_b128 v[178:181], v169 offset:49152
	ds_read_b128 v[182:185], v169 offset:50176
	ds_read_b128 v[204:207], v169 offset:51200
	ds_read_b128 v[208:211], v169 offset:52224
	ds_read_b128 v[212:215], v169 offset:53248
	ds_read_b128 v[216:219], v169 offset:54272
	ds_read_b128 v[222:225], v169 offset:55296
	ds_read_b128 v[226:229], v169 offset:56320
	global_load_lds_dwordx4 v[194:195], off
	v_lshl_add_u64 v[194:195], v[196:197], 0, s[26:27]
	s_mov_b32 m0, s51
	s_addc_u32 s31, s31, 0
	s_add_i32 s64, s64, s82
	global_load_lds_dwordx4 v[194:195], off
	v_lshl_add_u64 v[194:195], s[30:31], 0, v[170:171]
	s_mov_b32 m0, s64
	s_add_i32 s63, s64, 0x2000
	global_load_lds_dwordx4 v[194:195], off
	v_lshl_add_u64 v[194:195], s[30:31], 0, v[172:173]
	s_mov_b32 m0, s63
	v_readlane_b32 s26, v253, 39
	global_load_lds_dwordx4 v[194:195], off
	s_mov_b32 m0, s90
	v_readlane_b32 s27, v253, 40
	s_nop 4
	global_load_lds_dwordx4 v34, s[26:27]
	s_mov_b32 m0, s91
	s_nop 0
	global_load_lds_dwordx4 v192, s[26:27]
	s_waitcnt vmcnt(8)
	s_waitcnt lgkmcnt(0)
	s_barrier
	s_setprio 1
	s_waitcnt lgkmcnt(0)
	v_mfma_f32_16x16x128_f8f6f4 v[96:99], v[26:33], v[178:185], v[96:99]
	v_mfma_f32_16x16x128_f8f6f4 v[92:95], v[18:25], v[178:185], v[92:95]
	v_mfma_f32_16x16x128_f8f6f4 v[88:91], v[26:33], v[204:211], v[88:91]
	v_mfma_f32_16x16x128_f8f6f4 v[84:87], v[18:25], v[204:211], v[84:87]
	v_mfma_f32_16x16x128_f8f6f4 v[80:83], v[26:33], v[212:219], v[80:83]
	v_mfma_f32_16x16x128_f8f6f4 v[76:79], v[18:25], v[212:219], v[76:79]
	v_mfma_f32_16x16x128_f8f6f4 v[72:75], v[26:33], v[222:229], v[72:75]
	v_mfma_f32_16x16x128_f8f6f4 v[68:71], v[18:25], v[222:229], v[68:71]
	s_setprio 0
	s_setprio 1
	v_mfma_f32_16x16x128_f8f6f4 v[64:67], v[10:17], v[178:185], v[64:67]
	v_mfma_f32_16x16x128_f8f6f4 v[60:63], v[2:9], v[178:185], v[60:63]
	v_mfma_f32_16x16x128_f8f6f4 v[56:59], v[10:17], v[204:211], v[56:59]
	v_mfma_f32_16x16x128_f8f6f4 v[52:55], v[2:9], v[204:211], v[52:55]
	v_mfma_f32_16x16x128_f8f6f4 v[48:51], v[10:17], v[212:219], v[48:51]
	v_mfma_f32_16x16x128_f8f6f4 v[44:47], v[2:9], v[212:219], v[44:47]
	v_mfma_f32_16x16x128_f8f6f4 v[40:43], v[10:17], v[222:229], v[40:43]
	v_mfma_f32_16x16x128_f8f6f4 v[36:39], v[2:9], v[222:229], v[36:39]
	s_setprio 0
	s_barrier
	v_lshl_add_u64 v[18:19], s[26:27], 0, v[174:175]
	v_lshl_add_u64 v[20:21], s[26:27], 0, v[190:191]
	s_mov_b32 s75, 0
	s_mov_b64 s[30:31], 0
	s_branch .LBB0_955
	.p2align	6

.LBB0_1086:
	s_lshl_b32 s10, s51, 18
	s_add_u32 s10, s20, s10
	s_addc_u32 s11, s21, 0
	s_and_b64 s[16:17], s[4:5], exec
	s_cselect_b32 s54, s11, s31
	s_cselect_b32 s55, s10, s30
	s_lshl_b32 s14, s50, 18
	s_add_u32 s16, s15, s14
	s_addc_u32 s17, s26, 0
	s_and_b64 s[36:37], s[4:5], exec
	s_cselect_b32 s56, s17, s23
	s_cselect_b32 s57, s16, s22
	s_add_i32 s60, 0, 0x10000
	s_add_i32 s62, 0, 0x14000
	v_add_u32_e32 v198, s60, v196
	v_add_u32_e32 v199, s62, v196
	ds_read_b128 v[26:29], v198
	ds_read_b128 v[30:33], v198 offset:1024
	ds_read_b128 v[18:21], v198 offset:2048
	ds_read_b128 v[22:25], v198 offset:3072
	ds_read_b128 v[10:13], v199
	ds_read_b128 v[14:17], v199 offset:1024
	ds_read_b128 v[2:5], v199 offset:2048
	ds_read_b128 v[6:9], v199 offset:3072
	s_add_u32 s36, s30, 0x20080
	s_addc_u32 s37, s31, 0
	s_add_i32 s58, s41, 0xc000
	v_lshl_add_u64 v[174:175], s[36:37], 0, v[168:169]
	s_mov_b32 m0, s58
	s_add_i32 s59, s41, 0xe000
	ds_read_b128 v[200:203], v197
	ds_read_b128 v[204:207], v197 offset:1024
	ds_read_b128 v[222:225], v197 offset:2048
	ds_read_b128 v[226:229], v197 offset:3072
	ds_read_b128 v[230:233], v197 offset:4096
	ds_read_b128 v[234:237], v197 offset:5120
	ds_read_b128 v[238:241], v197 offset:6144
	ds_read_b128 v[242:245], v197 offset:7168
	global_load_lds_dwordx4 v[174:175], off
	v_lshl_add_u64 v[174:175], s[36:37], 0, v[166:167]
	s_mov_b32 m0, s59
	s_nop 0
	global_load_lds_dwordx4 v[174:175], off
	s_waitcnt vmcnt(8)
	s_waitcnt lgkmcnt(0)
	s_barrier
	s_setprio 1
	s_waitcnt lgkmcnt(0)
	v_mfma_f32_16x16x128_f8f6f4 v[160:163], v[26:33], v[200:207], 0
	v_mfma_f32_16x16x128_f8f6f4 v[156:159], v[18:25], v[200:207], 0
	v_mfma_f32_16x16x128_f8f6f4 v[152:155], v[26:33], v[222:229], 0
	v_mfma_f32_16x16x128_f8f6f4 v[148:151], v[18:25], v[222:229], 0
	v_mfma_f32_16x16x128_f8f6f4 v[144:147], v[26:33], v[230:237], 0
	v_mfma_f32_16x16x128_f8f6f4 v[140:143], v[18:25], v[230:237], 0
	v_mfma_f32_16x16x128_f8f6f4 v[136:139], v[26:33], v[238:245], 0
	v_mfma_f32_16x16x128_f8f6f4 v[132:135], v[18:25], v[238:245], 0
	s_setprio 0
	s_setprio 1
	v_mfma_f32_16x16x128_f8f6f4 v[128:131], v[10:17], v[200:207], 0
	v_mfma_f32_16x16x128_f8f6f4 v[124:127], v[2:9], v[200:207], 0
	v_mfma_f32_16x16x128_f8f6f4 v[120:123], v[10:17], v[222:229], 0
	v_mfma_f32_16x16x128_f8f6f4 v[116:119], v[2:9], v[222:229], 0
	v_mfma_f32_16x16x128_f8f6f4 v[112:115], v[10:17], v[230:237], 0
	v_mfma_f32_16x16x128_f8f6f4 v[108:111], v[2:9], v[230:237], 0
	v_mfma_f32_16x16x128_f8f6f4 v[104:107], v[10:17], v[238:245], 0
	v_mfma_f32_16x16x128_f8f6f4 v[100:103], v[2:9], v[238:245], 0
	s_setprio 0
	s_barrier
	s_add_i32 s60, s60, s40
	v_lshl_add_u64 v[174:175], s[22:23], 0, v[34:35]
	s_add_i32 s61, s60, 0x2000
	v_lshl_add_u64 v[178:179], v[174:175], 0, s[28:29]
	s_mov_b32 m0, s60
	v_lshl_add_u64 v[190:191], s[22:23], 0, v[164:165]
	s_add_u32 s36, s22, 0x20100
	ds_read_b128 v[200:203], v197 offset:16384
	ds_read_b128 v[204:207], v197 offset:17408
	ds_read_b128 v[222:225], v197 offset:18432
	ds_read_b128 v[226:229], v197 offset:19456
	ds_read_b128 v[230:233], v197 offset:20480
	ds_read_b128 v[234:237], v197 offset:21504
	ds_read_b128 v[238:241], v197 offset:22528
	ds_read_b128 v[242:245], v197 offset:23552
	global_load_lds_dwordx4 v[178:179], off
	v_lshl_add_u64 v[178:179], v[190:191], 0, s[28:29]
	s_mov_b32 m0, s61
	s_addc_u32 s37, s23, 0
	s_add_i32 s62, s62, s40
	global_load_lds_dwordx4 v[178:179], off
	v_lshl_add_u64 v[178:179], s[36:37], 0, v[34:35]
	s_mov_b32 m0, s62
	s_add_i32 s63, s62, 0x2000
	global_load_lds_dwordx4 v[178:179], off
	v_lshl_add_u64 v[178:179], s[36:37], 0, v[164:165]
	s_mov_b32 m0, s63
	v_lshl_add_u64 v[192:193], s[30:31], 0, v[168:169]
	global_load_lds_dwordx4 v[178:179], off
	v_lshl_add_u64 v[178:179], v[192:193], 0, s[28:29]
	s_mov_b32 m0, s41
	v_lshl_add_u64 v[194:195], s[30:31], 0, v[166:167]
	global_load_lds_dwordx4 v[178:179], off
	v_lshl_add_u64 v[178:179], v[194:195], 0, s[28:29]
	s_mov_b32 m0, s42
	s_nop 0
	global_load_lds_dwordx4 v[178:179], off
	s_waitcnt vmcnt(8)
	s_waitcnt lgkmcnt(0)
	s_barrier
	s_setprio 1
	s_waitcnt lgkmcnt(0)
	v_mfma_f32_16x16x128_f8f6f4 v[96:99], v[26:33], v[200:207], 0
	v_mfma_f32_16x16x128_f8f6f4 v[92:95], v[18:25], v[200:207], 0
	v_mfma_f32_16x16x128_f8f6f4 v[88:91], v[26:33], v[222:229], 0
	v_mfma_f32_16x16x128_f8f6f4 v[84:87], v[18:25], v[222:229], 0
	v_mfma_f32_16x16x128_f8f6f4 v[80:83], v[26:33], v[230:237], 0
	v_mfma_f32_16x16x128_f8f6f4 v[76:79], v[18:25], v[230:237], 0
	v_mfma_f32_16x16x128_f8f6f4 v[72:75], v[26:33], v[238:245], 0
	v_mfma_f32_16x16x128_f8f6f4 v[68:71], v[18:25], v[238:245], 0
	s_setprio 0
	s_setprio 1
	v_mfma_f32_16x16x128_f8f6f4 v[64:67], v[10:17], v[200:207], 0
	v_mfma_f32_16x16x128_f8f6f4 v[60:63], v[2:9], v[200:207], 0
	v_mfma_f32_16x16x128_f8f6f4 v[56:59], v[10:17], v[222:229], 0
	v_mfma_f32_16x16x128_f8f6f4 v[52:55], v[2:9], v[222:229], 0
	v_mfma_f32_16x16x128_f8f6f4 v[48:51], v[10:17], v[230:237], 0
	v_mfma_f32_16x16x128_f8f6f4 v[44:47], v[2:9], v[230:237], 0
	v_mfma_f32_16x16x128_f8f6f4 v[40:43], v[10:17], v[238:245], 0
	v_mfma_f32_16x16x128_f8f6f4 v[36:39], v[2:9], v[238:245], 0
	s_setprio 0
	s_barrier
	s_add_i32 s64, 0, 0x18000
	s_add_i32 s66, 0, 0x1c000
	v_add_u32_e32 v200, s64, v196
	v_add_u32_e32 v201, s66, v196
	ds_read_b128 v[26:29], v200
	ds_read_b128 v[30:33], v200 offset:1024
	ds_read_b128 v[18:21], v200 offset:2048
	ds_read_b128 v[22:25], v200 offset:3072
	ds_read_b128 v[10:13], v201
	ds_read_b128 v[14:17], v201 offset:1024
	ds_read_b128 v[2:5], v201 offset:2048
	ds_read_b128 v[6:9], v201 offset:3072
	s_add_u32 s36, s30, 0x20100
	s_addc_u32 s37, s31, 0
	s_mov_b32 m0, s43
	v_lshl_add_u64 v[178:179], s[36:37], 0, v[168:169]
	ds_read_b128 v[202:205], v197 offset:32768
	ds_read_b128 v[206:209], v197 offset:33792
	ds_read_b128 v[222:225], v197 offset:34816
	ds_read_b128 v[226:229], v197 offset:35840
	ds_read_b128 v[230:233], v197 offset:36864
	ds_read_b128 v[234:237], v197 offset:37888
	ds_read_b128 v[238:241], v197 offset:38912
	ds_read_b128 v[242:245], v197 offset:39936
	global_load_lds_dwordx4 v[178:179], off
	v_lshl_add_u64 v[178:179], s[36:37], 0, v[166:167]
	s_mov_b32 m0, s44
	s_nop 0
	global_load_lds_dwordx4 v[178:179], off
	s_waitcnt vmcnt(8)
	s_waitcnt lgkmcnt(0)
	s_barrier
	s_setprio 1
	s_waitcnt lgkmcnt(0)
	v_mfma_f32_16x16x128_f8f6f4 v[160:163], v[26:33], v[202:209], v[160:163]
	v_mfma_f32_16x16x128_f8f6f4 v[156:159], v[18:25], v[202:209], v[156:159]
	v_mfma_f32_16x16x128_f8f6f4 v[152:155], v[26:33], v[222:229], v[152:155]
	v_mfma_f32_16x16x128_f8f6f4 v[148:151], v[18:25], v[222:229], v[148:151]
	v_mfma_f32_16x16x128_f8f6f4 v[144:147], v[26:33], v[230:237], v[144:147]
	v_mfma_f32_16x16x128_f8f6f4 v[140:143], v[18:25], v[230:237], v[140:143]
	v_mfma_f32_16x16x128_f8f6f4 v[136:139], v[26:33], v[238:245], v[136:139]
	v_mfma_f32_16x16x128_f8f6f4 v[132:135], v[18:25], v[238:245], v[132:135]
	s_setprio 0
	s_setprio 1
	v_mfma_f32_16x16x128_f8f6f4 v[128:131], v[10:17], v[202:209], v[128:131]
	v_mfma_f32_16x16x128_f8f6f4 v[124:127], v[2:9], v[202:209], v[124:127]
	v_mfma_f32_16x16x128_f8f6f4 v[120:123], v[10:17], v[222:229], v[120:123]
	v_mfma_f32_16x16x128_f8f6f4 v[116:119], v[2:9], v[222:229], v[116:119]
	v_mfma_f32_16x16x128_f8f6f4 v[112:115], v[10:17], v[230:237], v[112:115]
	v_mfma_f32_16x16x128_f8f6f4 v[108:111], v[2:9], v[230:237], v[108:111]
	v_mfma_f32_16x16x128_f8f6f4 v[104:107], v[10:17], v[238:245], v[104:107]
	v_mfma_f32_16x16x128_f8f6f4 v[100:103], v[2:9], v[238:245], v[100:103]
	s_setprio 0
	s_barrier
	s_add_i32 s64, s64, s40
	s_mov_b64 s[24:25], 0x180
	s_add_i32 s65, s64, 0x2000
	v_lshl_add_u64 v[174:175], v[174:175], 0, s[24:25]
	s_mov_b32 m0, s64
	s_add_u32 s36, s22, 0x20180
	ds_read_b128 v[202:205], v197 offset:49152
	ds_read_b128 v[206:209], v197 offset:50176
	ds_read_b128 v[222:225], v197 offset:51200
	ds_read_b128 v[226:229], v197 offset:52224
	ds_read_b128 v[230:233], v197 offset:53248
	ds_read_b128 v[234:237], v197 offset:54272
	ds_read_b128 v[238:241], v197 offset:55296
	ds_read_b128 v[242:245], v197 offset:56320
	global_load_lds_dwordx4 v[174:175], off
	v_lshl_add_u64 v[174:175], v[190:191], 0, s[24:25]
	s_mov_b32 m0, s65
	s_addc_u32 s37, s23, 0
	s_add_i32 s66, s66, s40
	global_load_lds_dwordx4 v[174:175], off
	v_lshl_add_u64 v[174:175], s[36:37], 0, v[34:35]
	s_mov_b32 m0, s66
	s_add_i32 s67, s66, 0x2000
	global_load_lds_dwordx4 v[174:175], off
	v_lshl_add_u64 v[174:175], s[36:37], 0, v[164:165]
	s_mov_b32 m0, s67
	s_nop 0
	global_load_lds_dwordx4 v[174:175], off
	v_lshl_add_u64 v[174:175], v[192:193], 0, s[24:25]
	s_mov_b32 m0, s47
	s_nop 0
	global_load_lds_dwordx4 v[174:175], off
	v_lshl_add_u64 v[174:175], v[194:195], 0, s[24:25]
	s_mov_b32 m0, s48
	s_nop 0
	global_load_lds_dwordx4 v[174:175], off
	s_waitcnt vmcnt(8)
	s_waitcnt lgkmcnt(0)
	s_barrier
	s_setprio 1
	s_waitcnt lgkmcnt(0)
	v_mfma_f32_16x16x128_f8f6f4 v[96:99], v[26:33], v[202:209], v[96:99]
	v_mfma_f32_16x16x128_f8f6f4 v[92:95], v[18:25], v[202:209], v[92:95]
	v_mfma_f32_16x16x128_f8f6f4 v[88:91], v[26:33], v[222:229], v[88:91]
	v_mfma_f32_16x16x128_f8f6f4 v[84:87], v[18:25], v[222:229], v[84:87]
	v_mfma_f32_16x16x128_f8f6f4 v[80:83], v[26:33], v[230:237], v[80:83]
	v_mfma_f32_16x16x128_f8f6f4 v[76:79], v[18:25], v[230:237], v[76:79]
	v_mfma_f32_16x16x128_f8f6f4 v[72:75], v[26:33], v[238:245], v[72:75]
	v_mfma_f32_16x16x128_f8f6f4 v[68:71], v[18:25], v[238:245], v[68:71]
	s_setprio 0
	s_setprio 1
	v_mfma_f32_16x16x128_f8f6f4 v[64:67], v[10:17], v[202:209], v[64:67]
	v_mfma_f32_16x16x128_f8f6f4 v[60:63], v[2:9], v[202:209], v[60:63]
	v_mfma_f32_16x16x128_f8f6f4 v[56:59], v[10:17], v[222:229], v[56:59]
	v_mfma_f32_16x16x128_f8f6f4 v[52:55], v[2:9], v[222:229], v[52:55]
	v_mfma_f32_16x16x128_f8f6f4 v[48:51], v[10:17], v[230:237], v[48:51]
	v_mfma_f32_16x16x128_f8f6f4 v[44:47], v[2:9], v[230:237], v[44:47]
	v_mfma_f32_16x16x128_f8f6f4 v[40:43], v[10:17], v[238:245], v[40:43]
	v_mfma_f32_16x16x128_f8f6f4 v[36:39], v[2:9], v[238:245], v[36:39]
	s_setprio 0
	s_barrier
	s_add_u32 s30, s30, 0x20180
	s_addc_u32 s31, s31, 0
	s_add_u32 s68, s22, 0x200
	s_addc_u32 s69, s23, 0
	s_mov_b32 s70, 0
	.p2align	6
